# UP epilogue stage 2: last 16-row step's G load issued one step earlier into phase-local v[226:229], row factors in v230/v231/v240; plus IN/GATE second-half row-factor hoist
# speedup vs baseline: 1.0078x; 1.0001x over previous
.LBB0_1923:
	s_lshl_b32 s11, s18, 8
	v_lshl_or_b32 v222, s19, 8, v243
	s_add_i32 s11, s11, s51
	v_ashrrev_i32_e32 v223, 31, v222
	v_or_b32_e32 v220, s11, v1
	v_lshlrev_b64 v[206:207], 1, v[222:223]
	s_and_b32 s13, s11, 0xfc0
	v_lshl_add_u64 v[224:225], s[4:5], 0, v[206:207]
	s_movk_i32 s21, 0x2c00
	s_cmp_lg_u32 s13, 0
	v_ashrrev_i32_e32 v221, 31, v220
	v_mad_i64_i32 v[36:37], s[18:19], v220, s21, v[224:225]
	v_lshl_add_u64 v[202:203], v[220:221], 2, s[6:7]
	s_cselect_b64 vcc, -1, 0
	global_load_dwordx4 v[164:167], v[36:37], off
	global_load_dword v186, v[202:203], off
	global_load_dword v230, v[202:203], off offset:64
	global_load_dword v231, v[202:203], off offset:128
	global_load_dword v240, v[202:203], off offset:192
	v_cndmask_b32_e32 v36, 0, v242, vcc
	v_add_u32_e32 v36, s11, v36
	v_mov_b64_e32 v[204:205], s[4:5]
	v_mad_i64_i32 v[36:37], s[18:19], v36, s21, v[204:205]
	v_lshl_add_u64 v[216:217], v[36:37], 0, v[206:207]
	global_load_dwordx4 v[182:185], v[216:217], off
	v_lshlrev_b64 v[36:37], 2, v[222:223]
	v_lshl_add_u64 v[208:209], v[178:179], 0, v[36:37]
	v_lshl_add_u64 v[38:39], v[194:195], 0, v[36:37]
	global_load_dwordx4 v[116:119], v[208:209], off
	global_load_dwordx4 v[128:131], v[38:39], off
	v_lshl_add_u64 v[40:41], v[196:197], 0, v[36:37]
	v_lshl_add_u64 v[210:211], v[180:181], 0, v[36:37]
	global_load_dwordx4 v[120:123], v[40:41], off
	global_load_dwordx4 v[124:127], v[210:211], off
	global_load_dwordx4 v[44:47], v[208:209], off offset:16
	global_load_dwordx4 v[48:51], v[38:39], off offset:16
	s_nop 0
	global_load_dwordx4 v[36:39], v[40:41], off offset:16
	s_nop 0
	global_load_dwordx4 v[40:43], v[210:211], off offset:16
	v_sub_u32_e32 v170, v220, v1
	v_and_b32_e32 v187, 0xfff, v170
	v_cmp_ne_u32_e32 vcc, 0, v187
	s_mov_b32 s20, 0xffff0000
	v_or_b32_e32 v212, 16, v220
	v_cndmask_b32_e64 v187, 0, -1, vcc
	v_cndmask_b32_e64 v223, 0, v187, s[38:39]
	v_cndmask_b32_e64 v245, 0, v187, s[36:37]
	v_mad_i64_i32 v[168:169], s[18:19], v212, s21, v[224:225]
	v_ashrrev_i32_e32 v213, 31, v212
	global_load_dwordx4 v[168:171], v[168:169], off
	s_addk_i32 s11, 0x80
	s_and_b32 s13, s11, 0xfc0
	s_cmp_lg_u32 s13, 0
	s_mov_b32 s25, 0x800000
	s_movk_i32 s24, 0x7200
	s_waitcnt lgkmcnt(0)
	s_waitcnt vmcnt(14)
	v_mov_b32_dpp v193, v164 row_shr:2 row_mask:0xf bank_mask:0xf bound_ctrl:1
	v_mov_b32_dpp v191, v164 row_shr:1 row_mask:0xf bank_mask:0xf bound_ctrl:1
	v_mov_b32_dpp v219, v165 row_shr:2 row_mask:0xf bank_mask:0xf bound_ctrl:1
	s_waitcnt vmcnt(13)
	v_pk_mul_f32 v[188:189], v[158:159], v[186:187] op_sel_hi:[1,0]
	v_pk_mul_f32 v[158:159], v[156:157], v[186:187] op_sel_hi:[1,0]
	v_lshlrev_b32_e32 v156, 16, v164
	v_and_b32_e32 v157, 0xffff0000, v164
	v_mov_b32_dpp v215, v165 row_shr:1 row_mask:0xf bank_mask:0xf bound_ctrl:1
	s_waitcnt vmcnt(9)
	v_and_b32_dpp v238, v182, v223 row_ror:2 row_mask:0xf bank_mask:0xf bound_ctrl:1
	v_and_b32_dpp v237, v182, v245 row_ror:1 row_mask:0xf bank_mask:0xf bound_ctrl:1
	v_and_b32_dpp v247, v184, v245 row_ror:1 row_mask:0xf bank_mask:0xf bound_ctrl:1
	v_and_b32_dpp v248, v184, v223 row_ror:2 row_mask:0xf bank_mask:0xf bound_ctrl:1
	v_and_b32_dpp v249, v185, v245 row_ror:1 row_mask:0xf bank_mask:0xf bound_ctrl:1
	v_and_b32_dpp v250, v185, v223 row_ror:2 row_mask:0xf bank_mask:0xf bound_ctrl:1
	v_or_b32_sdwa v184, v238, v193 dst_sel:WORD_1 dst_unused:UNUSED_PAD src0_sel:DWORD src1_sel:DWORD
	v_bitop3_b32 v185, v238, s20, v193 bitop3:0xc8
	v_and_b32_dpp v239, v183, v245 row_ror:1 row_mask:0xf bank_mask:0xf bound_ctrl:1
	v_and_b32_dpp v246, v183, v223 row_ror:2 row_mask:0xf bank_mask:0xf bound_ctrl:1
	v_or_b32_sdwa v182, v237, v191 dst_sel:WORD_1 dst_unused:UNUSED_PAD src0_sel:DWORD src1_sel:DWORD
	v_bitop3_b32 v183, v237, s20, v191 bitop3:0xc8
	s_waitcnt vmcnt(8)
	v_pk_mul_f32 v[184:185], v[116:117], v[184:185]
	v_or_b32_sdwa v192, v246, v219 dst_sel:WORD_1 dst_unused:UNUSED_PAD src0_sel:DWORD src1_sel:DWORD
	s_waitcnt vmcnt(7)
	v_pk_fma_f32 v[182:183], v[128:129], v[182:183], v[184:185]
	v_bitop3_b32 v193, v246, s20, v219 bitop3:0xc8
	s_waitcnt vmcnt(6)
	v_pk_fma_f32 v[156:157], v[120:121], v[156:157], v[182:183]
	v_or_b32_sdwa v190, v239, v215 dst_sel:WORD_1 dst_unused:UNUSED_PAD src0_sel:DWORD src1_sel:DWORD
	v_bitop3_b32 v191, v239, s20, v215 bitop3:0xc8
	v_pk_mul_f32 v[192:193], v[118:119], v[192:193]
	s_waitcnt vmcnt(5)
	v_pk_add_f32 v[156:157], v[124:125], v[156:157]
	v_pk_mul_f32 v[162:163], v[162:163], v[186:187] op_sel_hi:[1,0]
	v_pk_mul_f32 v[160:161], v[160:161], v[186:187] op_sel_hi:[1,0]
	v_lshlrev_b32_e32 v186, 16, v165
	v_and_b32_e32 v187, 0xffff0000, v165
	v_pk_fma_f32 v[184:185], v[130:131], v[190:191], v[192:193]
	v_mul_f32_e32 v182, 0xbfb8aa3b, v156
	v_mul_f32_e32 v183, 0xbfb8aa3b, v157
	v_exp_f32_e32 v190, v182
	v_exp_f32_e32 v191, v183
	v_pk_fma_f32 v[182:183], v[122:123], v[186:187], v[184:185]
	v_mov_b32_dpp v233, v166 row_shr:2 row_mask:0xf bank_mask:0xf bound_ctrl:1
	v_pk_add_f32 v[182:183], v[126:127], v[182:183]
	v_add_f32_e32 v184, 1.0, v190
	v_mul_f32_e32 v186, 0xbfb8aa3b, v182
	v_mul_f32_e32 v187, 0xbfb8aa3b, v183
	v_exp_f32_e32 v186, v186
	v_exp_f32_e32 v187, v187
	v_add_f32_e32 v185, 1.0, v191
	v_rcp_f32_e32 v184, v184
	v_rcp_f32_e32 v185, v185
	v_add_f32_e32 v186, 1.0, v186
	v_add_f32_e32 v187, 1.0, v187
	v_rcp_f32_e32 v186, v186
	v_rcp_f32_e32 v187, v187
	v_pk_mul_f32 v[156:157], v[156:157], v[184:185]
	v_mov_b32_dpp v221, v166 row_shr:1 row_mask:0xf bank_mask:0xf bound_ctrl:1
	v_or_b32_sdwa v218, v248, v233 dst_sel:WORD_1 dst_unused:UNUSED_PAD src0_sel:DWORD src1_sel:DWORD
	v_bitop3_b32 v219, v248, s20, v233 bitop3:0xc8
	v_pk_mul_f32 v[156:157], v[156:157], v[160:161]
	v_pk_mul_f32 v[160:161], v[182:183], v[186:187]
	v_or_b32_sdwa v214, v247, v221 dst_sel:WORD_1 dst_unused:UNUSED_PAD src0_sel:DWORD src1_sel:DWORD
	v_bitop3_b32 v215, v247, s20, v221 bitop3:0xc8
	v_pk_mul_f32 v[160:161], v[160:161], v[162:163]
	s_waitcnt vmcnt(4)
	v_pk_mul_f32 v[162:163], v[44:45], v[218:219]
	v_lshlrev_b32_e32 v182, 16, v166
	s_waitcnt vmcnt(3)
	v_pk_fma_f32 v[162:163], v[48:49], v[214:215], v[162:163]
	v_and_b32_e32 v183, 0xffff0000, v166
	s_waitcnt vmcnt(2)
	v_pk_fma_f32 v[162:163], v[36:37], v[182:183], v[162:163]
	v_cvt_pk_bf16_f32 v156, v156, v157
	s_waitcnt vmcnt(1)
	v_pk_add_f32 v[162:163], v[40:41], v[162:163]
	v_mov_b32_dpp v235, v167 row_shr:2 row_mask:0xf bank_mask:0xf bound_ctrl:1
	v_mul_f32_e32 v157, 0xbfb8aa3b, v162
	v_exp_f32_e32 v182, v157
	v_mul_f32_e32 v157, 0xbfb8aa3b, v163
	v_exp_f32_e32 v183, v157
	v_mov_b32_dpp v236, v167 row_shr:1 row_mask:0xf bank_mask:0xf bound_ctrl:1
	v_or_b32_sdwa v234, v250, v235 dst_sel:WORD_1 dst_unused:UNUSED_PAD src0_sel:DWORD src1_sel:DWORD
	v_bitop3_b32 v235, v250, s20, v235 bitop3:0xc8
	v_or_b32_sdwa v232, v249, v236 dst_sel:WORD_1 dst_unused:UNUSED_PAD src0_sel:DWORD src1_sel:DWORD
	v_bitop3_b32 v233, v249, s20, v236 bitop3:0xc8
	v_cvt_pk_bf16_f32 v157, v160, v161
	v_add_f32_e32 v160, 1.0, v182
	v_add_f32_e32 v161, 1.0, v183
	v_pk_mul_f32 v[182:183], v[46:47], v[234:235]
	v_lshlrev_b32_e32 v184, 16, v167
	v_pk_fma_f32 v[182:183], v[50:51], v[232:233], v[182:183]
	v_and_b32_e32 v185, 0xffff0000, v167
	v_pk_fma_f32 v[182:183], v[38:39], v[184:185], v[182:183]
	v_rcp_f32_e32 v160, v160
	v_pk_add_f32 v[182:183], v[42:43], v[182:183]
	v_rcp_f32_e32 v161, v161
	v_mul_f32_e32 v184, 0xbfb8aa3b, v182
	v_mul_f32_e32 v185, 0xbfb8aa3b, v183
	v_exp_f32_e32 v184, v184
	v_exp_f32_e32 v185, v185
	v_pk_mul_f32 v[160:161], v[162:163], v[160:161]
	v_mov_b64_e32 v[218:219], s[2:3]
	v_add_f32_e32 v184, 1.0, v184
	v_add_f32_e32 v185, 1.0, v185
	v_rcp_f32_e32 v184, v184
	v_rcp_f32_e32 v185, v185
	v_pk_mul_f32 v[158:159], v[158:159], v[160:161]
	v_lshl_add_u64 v[214:215], v[212:213], 2, s[6:7]
	v_cvt_pk_bf16_f32 v158, v158, v159
	v_pk_mul_f32 v[160:161], v[182:183], v[184:185]
	v_sub_u32_e32 v183, v212, v1
	v_pk_mul_f32 v[160:161], v[188:189], v[160:161]
	v_and_b32_e32 v183, 0xfdf, v183
	v_cvt_pk_bf16_f32 v159, v160, v161
	v_mad_i64_i32 v[160:161], s[18:19], v220, s21, v[218:219]
	v_lshl_add_u64 v[162:163], v[160:161], 0, v[206:207]
	global_store_dwordx4 v[162:163], v[156:159], off
	v_mov_b32_e32 v182, v230
	v_cmp_ne_u32_e32 vcc, 0, v183
	s_waitcnt vmcnt(1)
	v_mov_b32_dpp v185, v168 row_shr:2 row_mask:0xf bank_mask:0xf bound_ctrl:1
	v_mov_b32_dpp v191, v169 row_shr:1 row_mask:0xf bank_mask:0xf bound_ctrl:1
	v_cndmask_b32_e64 v183, 0, -1, vcc
	v_cndmask_b32_e64 v213, 0, v183, s[38:39]
	v_cndmask_b32_e64 v221, 0, v183, s[36:37]
	v_mov_b32_dpp v183, v168 row_shr:1 row_mask:0xf bank_mask:0xf bound_ctrl:1
	v_and_b32_dpp v189, v164, v213 row_ror:2 row_mask:0xf bank_mask:0xf bound_ctrl:1
	v_and_b32_dpp v187, v164, v221 row_ror:1 row_mask:0xf bank_mask:0xf bound_ctrl:1
	v_or_b32_sdwa v164, v189, v185 dst_sel:WORD_1 dst_unused:UNUSED_PAD src0_sel:DWORD src1_sel:DWORD
	v_mov_b32_dpp v193, v169 row_shr:2 row_mask:0xf bank_mask:0xf bound_ctrl:1
	v_and_b32_dpp v233, v165, v221 row_ror:1 row_mask:0xf bank_mask:0xf bound_ctrl:1
	v_and_b32_dpp v234, v165, v213 row_ror:2 row_mask:0xf bank_mask:0xf bound_ctrl:1
	v_mov_b32_dpp v235, v170 row_shr:1 row_mask:0xf bank_mask:0xf bound_ctrl:1
	v_and_b32_dpp v237, v166, v221 row_ror:1 row_mask:0xf bank_mask:0xf bound_ctrl:1
	v_bitop3_b32 v165, v189, s20, v185 bitop3:0xc8
	v_or_b32_sdwa v184, v187, v183 dst_sel:WORD_1 dst_unused:UNUSED_PAD src0_sel:DWORD src1_sel:DWORD
	v_or_b32_sdwa v186, v233, v191 dst_sel:WORD_1 dst_unused:UNUSED_PAD src0_sel:DWORD src1_sel:DWORD
	v_or_b32_sdwa v188, v234, v193 dst_sel:WORD_1 dst_unused:UNUSED_PAD src0_sel:DWORD src1_sel:DWORD
	v_or_b32_sdwa v190, v237, v235 dst_sel:WORD_1 dst_unused:UNUSED_PAD src0_sel:DWORD src1_sel:DWORD
	v_bitop3_b32 v185, v187, s20, v183 bitop3:0xc8
	v_bitop3_b32 v189, v234, s20, v193 bitop3:0xc8
	v_bitop3_b32 v187, v233, s20, v191 bitop3:0xc8
	v_bitop3_b32 v191, v237, s20, v235 bitop3:0xc8
	v_mov_b32_dpp v236, v170 row_shr:2 row_mask:0xf bank_mask:0xf bound_ctrl:1
	v_and_b32_dpp v238, v166, v213 row_ror:2 row_mask:0xf bank_mask:0xf bound_ctrl:1
	v_or_b32_sdwa v166, v238, v236 dst_sel:WORD_1 dst_unused:UNUSED_PAD src0_sel:DWORD src1_sel:DWORD
	v_and_b32_dpp v247, v167, v221 row_ror:1 row_mask:0xf bank_mask:0xf bound_ctrl:1
	v_and_b32_dpp v248, v167, v213 row_ror:2 row_mask:0xf bank_mask:0xf bound_ctrl:1
	v_bitop3_b32 v167, v238, s20, v236 bitop3:0xc8
	v_mov_b32_dpp v246, v171 row_shr:2 row_mask:0xf bank_mask:0xf bound_ctrl:1
	v_mov_b32_dpp v239, v171 row_shr:1 row_mask:0xf bank_mask:0xf bound_ctrl:1
	v_or_b32_sdwa v232, v248, v246 dst_sel:WORD_1 dst_unused:UNUSED_PAD src0_sel:DWORD src1_sel:DWORD
	v_bitop3_b32 v233, v248, s20, v246 bitop3:0xc8
	v_or_b32_sdwa v192, v247, v239 dst_sel:WORD_1 dst_unused:UNUSED_PAD src0_sel:DWORD src1_sel:DWORD
	v_bitop3_b32 v193, v247, s20, v239 bitop3:0xc8
	v_or_b32_e32 v160, 32, v220
	v_mad_i64_i32 v[156:157], s[18:19], v160, s21, v[224:225]
	global_load_dwordx4 v[156:159], v[156:157], off
	v_add_u32_e32 v251, 16, v160
	v_mad_i64_i32 v[226:227], s[100:101], v251, s21, v[224:225]
	global_load_dwordx4 v[226:229], v[226:227], off
	v_ashrrev_i32_e32 v161, 31, v160
	s_waitcnt lgkmcnt(0)
	v_pk_mul_f32 v[234:235], v[150:151], v[182:183] op_sel_hi:[1,0]
	v_pk_mul_f32 v[150:151], v[116:117], v[164:165]
	v_pk_mul_f32 v[154:155], v[154:155], v[182:183] op_sel_hi:[1,0]
	v_pk_mul_f32 v[152:153], v[152:153], v[182:183] op_sel_hi:[1,0]
	v_pk_fma_f32 v[150:151], v[128:129], v[184:185], v[150:151]
	v_lshlrev_b32_e32 v164, 16, v168
	v_and_b32_e32 v165, 0xffff0000, v168
	v_pk_mul_f32 v[148:149], v[148:149], v[182:183] op_sel_hi:[1,0]
	v_pk_mul_f32 v[182:183], v[118:119], v[188:189]
	v_pk_fma_f32 v[150:151], v[120:121], v[164:165], v[150:151]
	v_pk_fma_f32 v[182:183], v[130:131], v[186:187], v[182:183]
	v_lshlrev_b32_e32 v184, 16, v169
	v_and_b32_e32 v185, 0xffff0000, v169
	v_pk_add_f32 v[150:151], v[124:125], v[150:151]
	v_pk_fma_f32 v[182:183], v[122:123], v[184:185], v[182:183]
	v_mul_f32_e32 v164, 0xbfb8aa3b, v150
	v_mul_f32_e32 v165, 0xbfb8aa3b, v151
	v_pk_add_f32 v[182:183], v[126:127], v[182:183]
	v_exp_f32_e32 v164, v164
	v_exp_f32_e32 v165, v165
	v_mul_f32_e32 v184, 0xbfb8aa3b, v182
	v_mul_f32_e32 v185, 0xbfb8aa3b, v183
	v_exp_f32_e32 v184, v184
	v_exp_f32_e32 v185, v185
	v_add_f32_e32 v164, 1.0, v164
	v_add_f32_e32 v165, 1.0, v165
	v_rcp_f32_e32 v164, v164
	v_rcp_f32_e32 v165, v165
	v_add_f32_e32 v184, 1.0, v184
	v_add_f32_e32 v185, 1.0, v185
	v_rcp_f32_e32 v184, v184
	v_rcp_f32_e32 v185, v185
	v_pk_mul_f32 v[150:151], v[150:151], v[164:165]
	v_lshlrev_b32_e32 v164, 16, v170
	v_pk_mul_f32 v[150:151], v[150:151], v[152:153]
	v_pk_mul_f32 v[152:153], v[182:183], v[184:185]
	v_and_b32_e32 v165, 0xffff0000, v170
	v_pk_mul_f32 v[152:153], v[152:153], v[154:155]
	v_pk_mul_f32 v[154:155], v[44:45], v[166:167]
	v_cvt_pk_bf16_f32 v150, v150, v151
	v_pk_fma_f32 v[154:155], v[48:49], v[190:191], v[154:155]
	v_lshlrev_b32_e32 v166, 16, v171
	v_pk_fma_f32 v[154:155], v[36:37], v[164:165], v[154:155]
	v_and_b32_e32 v167, 0xffff0000, v171
	v_pk_add_f32 v[154:155], v[40:41], v[154:155]
	s_nop 0
	v_mul_f32_e32 v151, 0xbfb8aa3b, v154
	v_exp_f32_e32 v164, v151
	v_mul_f32_e32 v151, 0xbfb8aa3b, v155
	v_exp_f32_e32 v165, v151
	v_cvt_pk_bf16_f32 v151, v152, v153
	v_add_f32_e32 v152, 1.0, v164
	v_rcp_f32_e32 v152, v152
	v_add_f32_e32 v153, 1.0, v165
	v_pk_mul_f32 v[164:165], v[46:47], v[232:233]
	v_rcp_f32_e32 v153, v153
	v_pk_fma_f32 v[164:165], v[50:51], v[192:193], v[164:165]
	v_pk_mul_f32 v[152:153], v[154:155], v[152:153]
	v_pk_fma_f32 v[164:165], v[38:39], v[166:167], v[164:165]
	v_pk_mul_f32 v[148:149], v[148:149], v[152:153]
	v_pk_add_f32 v[164:165], v[42:43], v[164:165]
	v_cvt_pk_bf16_f32 v152, v148, v149
	v_mul_f32_e32 v166, 0xbfb8aa3b, v164
	v_mul_f32_e32 v167, 0xbfb8aa3b, v165
	v_exp_f32_e32 v166, v166
	v_exp_f32_e32 v167, v167
	v_sub_u32_e32 v155, v160, v1
	v_and_b32_e32 v155, 0xfff, v155
	v_add_f32_e32 v166, 1.0, v166
	v_add_f32_e32 v167, 1.0, v167
	v_rcp_f32_e32 v166, v166
	v_rcp_f32_e32 v167, v167
	v_cmp_ne_u32_e32 vcc, 0, v155
	v_pk_mul_f32 v[148:149], v[164:165], v[166:167]
	s_nop 0
	v_pk_mul_f32 v[148:149], v[234:235], v[148:149]
	v_cndmask_b32_e64 v155, 0, -1, vcc
	v_cvt_pk_bf16_f32 v153, v148, v149
	v_mad_i64_i32 v[148:149], s[18:19], v212, s21, v[218:219]
	v_lshl_add_u64 v[148:149], v[148:149], 0, v[206:207]
	global_store_dwordx4 v[148:149], v[150:153], off
	s_cselect_b64 vcc, -1, 0
	s_nop 0
	v_lshl_add_u64 v[150:151], v[160:161], 2, s[6:7]
	v_mov_b32_e32 v154, v231
	v_or_b32_e32 v152, 48, v220
	v_mad_i64_i32 v[164:165], s[18:19], v152, s21, v[224:225]
	v_cndmask_b32_e64 v161, 0, v155, s[38:39]
	s_waitcnt vmcnt(1)
	v_mov_b32_e32 v182, v226
	v_mov_b32_e32 v183, v227
	v_mov_b32_e32 v184, v228
	v_mov_b32_e32 v185, v229
	s_nop 1
	v_cndmask_b32_e64 v164, 0, v155, s[36:37]
	v_mov_b32_dpp v165, v156 row_shr:2 row_mask:0xf bank_mask:0xf bound_ctrl:1
	v_and_b32_dpp v187, v168, v161 row_ror:2 row_mask:0xf bank_mask:0xf bound_ctrl:1
	v_mov_b32_dpp v155, v156 row_shr:1 row_mask:0xf bank_mask:0xf bound_ctrl:1
	v_and_b32_dpp v167, v168, v164 row_ror:1 row_mask:0xf bank_mask:0xf bound_ctrl:1
	v_or_b32_sdwa v168, v187, v165 dst_sel:WORD_1 dst_unused:UNUSED_PAD src0_sel:DWORD src1_sel:DWORD
	v_and_b32_dpp v193, v169, v164 row_ror:1 row_mask:0xf bank_mask:0xf bound_ctrl:1
	v_and_b32_dpp v233, v169, v161 row_ror:2 row_mask:0xf bank_mask:0xf bound_ctrl:1
	v_bitop3_b32 v169, v187, s20, v165 bitop3:0xc8
	v_or_b32_sdwa v166, v167, v155 dst_sel:WORD_1 dst_unused:UNUSED_PAD src0_sel:DWORD src1_sel:DWORD
	v_bitop3_b32 v167, v167, s20, v155 bitop3:0xc8
	v_pk_mul_f32 v[168:169], v[116:117], v[168:169]
	v_mov_b32_dpp v189, v157 row_shr:2 row_mask:0xf bank_mask:0xf bound_ctrl:1
	v_pk_fma_f32 v[166:167], v[128:129], v[166:167], v[168:169]
	v_lshlrev_b32_e32 v168, 16, v156
	v_and_b32_e32 v169, 0xffff0000, v156
	v_pk_fma_f32 v[166:167], v[120:121], v[168:169], v[166:167]
	v_mov_b32_dpp v191, v157 row_shr:1 row_mask:0xf bank_mask:0xf bound_ctrl:1
	v_pk_add_f32 v[166:167], v[124:125], v[166:167]
	v_or_b32_sdwa v188, v233, v189 dst_sel:WORD_1 dst_unused:UNUSED_PAD src0_sel:DWORD src1_sel:DWORD
	v_bitop3_b32 v189, v233, s20, v189 bitop3:0xc8
	v_mul_f32_e32 v165, 0xbfb8aa3b, v167
	v_or_b32_sdwa v186, v193, v191 dst_sel:WORD_1 dst_unused:UNUSED_PAD src0_sel:DWORD src1_sel:DWORD
	v_bitop3_b32 v187, v193, s20, v191 bitop3:0xc8
	v_exp_f32_e32 v165, v165
	v_pk_mul_f32 v[168:169], v[118:119], v[188:189]
	v_mov_b32_dpp v235, v158 row_shr:2 row_mask:0xf bank_mask:0xf bound_ctrl:1
	v_pk_fma_f32 v[168:169], v[130:131], v[186:187], v[168:169]
	v_lshlrev_b32_e32 v186, 16, v157
	v_and_b32_e32 v187, 0xffff0000, v157
	v_pk_fma_f32 v[168:169], v[122:123], v[186:187], v[168:169]
	v_and_b32_dpp v237, v170, v161 row_ror:2 row_mask:0xf bank_mask:0xf bound_ctrl:1
	v_pk_add_f32 v[168:169], v[126:127], v[168:169]
	v_mov_b32_dpp v234, v158 row_shr:1 row_mask:0xf bank_mask:0xf bound_ctrl:1
	v_mul_f32_e32 v186, 0xbfb8aa3b, v169
	v_exp_f32_e32 v187, v186
	v_and_b32_dpp v236, v170, v164 row_ror:1 row_mask:0xf bank_mask:0xf bound_ctrl:1
	v_or_b32_sdwa v170, v237, v235 dst_sel:WORD_1 dst_unused:UNUSED_PAD src0_sel:DWORD src1_sel:DWORD
	v_and_b32_dpp v246, v171, v164 row_ror:1 row_mask:0xf bank_mask:0xf bound_ctrl:1
	v_and_b32_dpp v247, v171, v161 row_ror:2 row_mask:0xf bank_mask:0xf bound_ctrl:1
	v_bitop3_b32 v171, v237, s20, v235 bitop3:0xc8
	v_or_b32_sdwa v190, v236, v234 dst_sel:WORD_1 dst_unused:UNUSED_PAD src0_sel:DWORD src1_sel:DWORD
	v_bitop3_b32 v191, v236, s20, v234 bitop3:0xc8
	v_mov_b32_dpp v239, v159 row_shr:2 row_mask:0xf bank_mask:0xf bound_ctrl:1
	v_mov_b32_dpp v238, v159 row_shr:1 row_mask:0xf bank_mask:0xf bound_ctrl:1
	v_or_b32_sdwa v232, v247, v239 dst_sel:WORD_1 dst_unused:UNUSED_PAD src0_sel:DWORD src1_sel:DWORD
	v_bitop3_b32 v233, v247, s20, v239 bitop3:0xc8
	v_or_b32_sdwa v192, v246, v238 dst_sel:WORD_1 dst_unused:UNUSED_PAD src0_sel:DWORD src1_sel:DWORD
	v_bitop3_b32 v193, v246, s20, v238 bitop3:0xc8
	v_ashrrev_i32_e32 v153, 31, v152
	s_waitcnt lgkmcnt(0)
	v_pk_mul_f32 v[146:147], v[146:147], v[154:155] op_sel_hi:[1,0]
	v_pk_mul_f32 v[144:145], v[144:145], v[154:155] op_sel_hi:[1,0]
	v_pk_mul_f32 v[142:143], v[142:143], v[154:155] op_sel_hi:[1,0]
	v_mul_f32_e32 v155, 0xbfb8aa3b, v166
	v_exp_f32_e32 v155, v155
	v_mov_b32_dpp v188, v184 row_shr:2 row_mask:0xf bank_mask:0xf bound_ctrl:1
	v_pk_mul_f32 v[140:141], v[140:141], v[154:155] op_sel_hi:[1,0]
	v_add_f32_e32 v154, 1.0, v155
	v_add_f32_e32 v155, 1.0, v165
	v_mul_f32_e32 v165, 0xbfb8aa3b, v168
	v_exp_f32_e32 v165, v165
	v_rcp_f32_e32 v154, v154
	v_rcp_f32_e32 v155, v155
	v_add_f32_e32 v165, 1.0, v165
	v_rcp_f32_e32 v186, v165
	v_add_f32_e32 v165, 1.0, v187
	v_rcp_f32_e32 v187, v165
	v_pk_mul_f32 v[154:155], v[166:167], v[154:155]
	v_lshlrev_b32_e32 v166, 16, v158
	v_pk_mul_f32 v[144:145], v[154:155], v[144:145]
	v_pk_mul_f32 v[154:155], v[168:169], v[186:187]
	v_and_b32_e32 v167, 0xffff0000, v158
	v_pk_mul_f32 v[146:147], v[154:155], v[146:147]
	v_pk_mul_f32 v[154:155], v[44:45], v[170:171]
	v_cvt_pk_bf16_f32 v144, v144, v145
	v_pk_fma_f32 v[154:155], v[48:49], v[190:191], v[154:155]
	v_lshlrev_b32_e32 v168, 16, v159
	v_pk_fma_f32 v[154:155], v[36:37], v[166:167], v[154:155]
	v_and_b32_e32 v169, 0xffff0000, v159
	v_pk_add_f32 v[154:155], v[40:41], v[154:155]
	v_mov_b32_dpp v187, v184 row_shr:1 row_mask:0xf bank_mask:0xf bound_ctrl:1
	v_mul_f32_e32 v145, 0xbfb8aa3b, v154
	v_exp_f32_e32 v165, v145
	v_mul_f32_e32 v145, 0xbfb8aa3b, v155
	v_exp_f32_e32 v166, v145
	v_cvt_pk_bf16_f32 v145, v146, v147
	v_add_f32_e32 v146, 1.0, v165
	v_rcp_f32_e32 v146, v146
	v_add_f32_e32 v147, 1.0, v166
	v_pk_mul_f32 v[166:167], v[46:47], v[232:233]
	v_rcp_f32_e32 v147, v147
	v_pk_fma_f32 v[166:167], v[50:51], v[192:193], v[166:167]
	v_mov_b32_dpp v192, v185 row_shr:2 row_mask:0xf bank_mask:0xf bound_ctrl:1
	v_pk_fma_f32 v[166:167], v[38:39], v[168:169], v[166:167]
	v_pk_mul_f32 v[146:147], v[154:155], v[146:147]
	v_pk_add_f32 v[166:167], v[42:43], v[166:167]
	v_pk_mul_f32 v[140:141], v[140:141], v[146:147]
	v_mul_f32_e32 v165, 0xbfb8aa3b, v166
	v_exp_f32_e32 v165, v165
	v_mul_f32_e32 v168, 0xbfb8aa3b, v167
	v_exp_f32_e32 v169, v168
	v_cvt_pk_bf16_f32 v146, v140, v141
	v_add_f32_e32 v165, 1.0, v165
	v_rcp_f32_e32 v168, v165
	v_add_f32_e32 v165, 1.0, v169
	v_rcp_f32_e32 v169, v165
	v_mov_b32_dpp v155, v157 row_ror:1 row_mask:0xf bank_mask:0xf bound_ctrl:1
	v_cndmask_b32_e64 v171, 0, v155, s[36:37]
	v_mov_b32_dpp v157, v157 row_ror:2 row_mask:0xf bank_mask:0xf bound_ctrl:1
	v_pk_mul_f32 v[140:141], v[166:167], v[168:169]
	v_mov_b32_dpp v155, v158 row_ror:1 row_mask:0xf bank_mask:0xf bound_ctrl:1
	v_pk_mul_f32 v[140:141], v[142:143], v[140:141]
	v_mov_b32_dpp v168, v158 row_ror:2 row_mask:0xf bank_mask:0xf bound_ctrl:1
	v_cvt_pk_bf16_f32 v147, v140, v141
	v_mad_i64_i32 v[140:141], s[18:19], v160, s21, v[218:219]
	v_lshl_add_u64 v[142:143], v[140:141], 0, v[206:207]
	global_store_dwordx4 v[142:143], v[144:147], off
	v_cndmask_b32_e64 v189, 0, v155, s[36:37]
	v_mov_b32_dpp v155, v159 row_ror:1 row_mask:0xf bank_mask:0xf bound_ctrl:1
	v_lshl_add_u64 v[144:145], v[152:153], 2, s[6:7]
	v_mov_b32_e32 v140, v240
	v_mov_b32_dpp v153, v156 row_ror:2 row_mask:0xf bank_mask:0xf bound_ctrl:1
	v_mov_b32_dpp v146, v156 row_ror:1 row_mask:0xf bank_mask:0xf bound_ctrl:1
	v_mov_b32_dpp v147, v182 row_shr:2 row_mask:0xf bank_mask:0xf bound_ctrl:1
	v_cndmask_b32_e64 v153, 0, v153, s[38:39]
	v_mov_b32_dpp v141, v182 row_shr:1 row_mask:0xf bank_mask:0xf bound_ctrl:1
	v_cndmask_b32_e64 v165, 0, v146, s[36:37]
	v_or_b32_sdwa v154, v153, v147 dst_sel:WORD_1 dst_unused:UNUSED_PAD src0_sel:DWORD src1_sel:DWORD
	v_mov_b32_dpp v169, v183 row_shr:1 row_mask:0xf bank_mask:0xf bound_ctrl:1
	v_mov_b32_dpp v167, v183 row_shr:2 row_mask:0xf bank_mask:0xf bound_ctrl:1
	v_cndmask_b32_e64 v157, 0, v157, s[38:39]
	v_cndmask_b32_e64 v190, 0, v168, s[38:39]
	v_mov_b32_dpp v159, v159 row_ror:2 row_mask:0xf bank_mask:0xf bound_ctrl:1
	v_cndmask_b32_e64 v193, 0, v155, s[36:37]
	v_bitop3_b32 v155, v153, s20, v147 bitop3:0xc8
	v_or_b32_sdwa v146, v165, v141 dst_sel:WORD_1 dst_unused:UNUSED_PAD src0_sel:DWORD src1_sel:DWORD
	v_or_b32_sdwa v156, v171, v169 dst_sel:WORD_1 dst_unused:UNUSED_PAD src0_sel:DWORD src1_sel:DWORD
	v_or_b32_sdwa v166, v157, v167 dst_sel:WORD_1 dst_unused:UNUSED_PAD src0_sel:DWORD src1_sel:DWORD
	v_or_b32_sdwa v158, v189, v187 dst_sel:WORD_1 dst_unused:UNUSED_PAD src0_sel:DWORD src1_sel:DWORD
	v_or_b32_sdwa v168, v190, v188 dst_sel:WORD_1 dst_unused:UNUSED_PAD src0_sel:DWORD src1_sel:DWORD
	v_cndmask_b32_e64 v232, 0, v159, s[38:39]
	v_bitop3_b32 v147, v165, s20, v141 bitop3:0xc8
	v_bitop3_b32 v167, v157, s20, v167 bitop3:0xc8
	v_bitop3_b32 v157, v171, s20, v169 bitop3:0xc8
	v_bitop3_b32 v169, v190, s20, v188 bitop3:0xc8
	v_bitop3_b32 v159, v189, s20, v187 bitop3:0xc8
	v_mov_b32_dpp v191, v185 row_shr:1 row_mask:0xf bank_mask:0xf bound_ctrl:1
	v_or_b32_sdwa v186, v232, v192 dst_sel:WORD_1 dst_unused:UNUSED_PAD src0_sel:DWORD src1_sel:DWORD
	v_bitop3_b32 v187, v232, s20, v192 bitop3:0xc8
	v_or_b32_sdwa v170, v193, v191 dst_sel:WORD_1 dst_unused:UNUSED_PAD src0_sel:DWORD src1_sel:DWORD
	v_bitop3_b32 v171, v193, s20, v191 bitop3:0xc8
	v_add_u32_e32 v165, 0x80, v220
	s_waitcnt lgkmcnt(0)
	v_pk_mul_f32 v[188:189], v[134:135], v[140:141] op_sel_hi:[1,0]
	v_pk_mul_f32 v[134:135], v[116:117], v[154:155]
	v_pk_mul_f32 v[138:139], v[138:139], v[140:141] op_sel_hi:[1,0]
	v_pk_fma_f32 v[134:135], v[128:129], v[146:147], v[134:135]
	v_lshlrev_b32_e32 v146, 16, v182
	v_and_b32_e32 v147, 0xffff0000, v182
	v_pk_fma_f32 v[134:135], v[120:121], v[146:147], v[134:135]
	v_pk_mul_f32 v[136:137], v[136:137], v[140:141] op_sel_hi:[1,0]
	v_pk_add_f32 v[134:135], v[124:125], v[134:135]
	v_lshlrev_b32_e32 v154, 16, v183
	v_mul_f32_e32 v141, 0xbfb8aa3b, v134
	v_exp_f32_e32 v146, v141
	v_mul_f32_e32 v141, 0xbfb8aa3b, v135
	v_exp_f32_e32 v147, v141
	v_pk_mul_f32 v[140:141], v[132:133], v[140:141] op_sel_hi:[1,0]
	v_add_f32_e32 v132, 1.0, v146
	v_and_b32_e32 v155, 0xffff0000, v183
	v_add_f32_e32 v133, 1.0, v147
	v_pk_mul_f32 v[146:147], v[118:119], v[166:167]
	v_rcp_f32_e32 v132, v132
	v_pk_fma_f32 v[146:147], v[130:131], v[156:157], v[146:147]
	v_rcp_f32_e32 v133, v133
	v_pk_fma_f32 v[146:147], v[122:123], v[154:155], v[146:147]
	v_pk_mul_f32 v[132:133], v[134:135], v[132:133]
	v_pk_add_f32 v[146:147], v[126:127], v[146:147]
	v_pk_mul_f32 v[132:133], v[132:133], v[136:137]
	v_mul_f32_e32 v153, 0xbfb8aa3b, v146
	v_exp_f32_e32 v153, v153
	v_mul_f32_e32 v154, 0xbfb8aa3b, v147
	v_exp_f32_e32 v155, v154
	v_pk_mul_f32 v[136:137], v[44:45], v[168:169]
	v_add_f32_e32 v153, 1.0, v153
	v_rcp_f32_e32 v154, v153
	v_add_f32_e32 v153, 1.0, v155
	v_rcp_f32_e32 v155, v153
	v_pk_fma_f32 v[136:137], v[48:49], v[158:159], v[136:137]
	v_cvt_pk_bf16_f32 v132, v132, v133
	v_add_u32_e32 v159, 0x90, v220
	v_pk_mul_f32 v[134:135], v[146:147], v[154:155]
	v_lshlrev_b32_e32 v146, 16, v185
	v_pk_mul_f32 v[134:135], v[134:135], v[138:139]
	v_lshlrev_b32_e32 v138, 16, v184
	v_and_b32_e32 v139, 0xffff0000, v184
	v_pk_fma_f32 v[136:137], v[36:37], v[138:139], v[136:137]
	v_and_b32_e32 v147, 0xffff0000, v185
	v_pk_add_f32 v[136:137], v[40:41], v[136:137]
	s_nop 0
	v_mul_f32_e32 v133, 0xbfb8aa3b, v136
	v_exp_f32_e32 v138, v133
	v_mul_f32_e32 v133, 0xbfb8aa3b, v137
	v_exp_f32_e32 v139, v133
	v_cvt_pk_bf16_f32 v133, v134, v135
	v_add_f32_e32 v134, 1.0, v138
	v_rcp_f32_e32 v134, v134
	v_add_f32_e32 v135, 1.0, v139
	v_pk_mul_f32 v[138:139], v[46:47], v[186:187]
	v_rcp_f32_e32 v135, v135
	v_pk_fma_f32 v[138:139], v[50:51], v[170:171], v[138:139]
	v_pk_mul_f32 v[134:135], v[136:137], v[134:135]
	v_pk_fma_f32 v[138:139], v[38:39], v[146:147], v[138:139]
	v_pk_mul_f32 v[134:135], v[140:141], v[134:135]
	v_pk_add_f32 v[138:139], v[42:43], v[138:139]
	v_cvt_pk_bf16_f32 v134, v134, v135
	v_mul_f32_e32 v146, 0xbfb8aa3b, v138
	v_mul_f32_e32 v147, 0xbfb8aa3b, v139
	v_exp_f32_e32 v146, v146
	v_exp_f32_e32 v147, v147
	v_add_f32_e32 v146, 1.0, v146
	v_add_f32_e32 v147, 1.0, v147
	v_rcp_f32_e32 v146, v146
	v_rcp_f32_e32 v147, v147
	s_nop 0
	v_pk_mul_f32 v[136:137], v[138:139], v[146:147]
	s_nop 0
	v_pk_mul_f32 v[136:137], v[188:189], v[136:137]
	v_sub_u32_e32 v139, v165, v1
	v_cvt_pk_bf16_f32 v135, v136, v137
	v_mad_i64_i32 v[136:137], s[18:19], v152, s21, v[218:219]
	v_lshl_add_u64 v[136:137], v[136:137], 0, v[206:207]
	global_store_dwordx4 v[136:137], v[132:135], off
	v_and_b32_e32 v139, 0xfff, v139
	s_nop 0
	v_cndmask_b32_e32 v132, 0, v242, vcc
	v_add_u32_e32 v132, s11, v132
	v_mad_i64_i32 v[132:133], s[18:19], v132, s21, v[204:205]
	v_mad_i64_i32 v[134:135], s[18:19], v165, s21, v[224:225]
	global_load_dwordx4 v[166:169], v[134:135], off
	v_lshl_add_u64 v[140:141], v[132:133], 0, v[206:207]
	global_load_dwordx4 v[182:185], v[140:141], off
	global_load_dword v138, v[202:203], off offset:512
	global_load_dword v230, v[202:203], off offset:576
	global_load_dword v231, v[202:203], off offset:640
	global_load_dword v240, v[202:203], off offset:704
	v_cmp_ne_u32_e32 vcc, 0, v139
	v_mad_i64_i32 v[132:133], s[18:19], v159, s21, v[224:225]
	s_nop 0
	v_cndmask_b32_e64 v139, 0, -1, vcc
	v_cndmask_b32_e64 v157, 0, v139, s[38:39]
	v_cndmask_b32_e64 v158, 0, v139, s[36:37]
	global_load_dwordx4 v[132:135], v[132:133], off
	s_waitcnt lgkmcnt(0)
	s_waitcnt vmcnt(6)
	v_mov_b32_dpp v147, v166 row_shr:2 row_mask:0xf bank_mask:0xf bound_ctrl:1
	s_waitcnt vmcnt(5)
	v_and_b32_dpp v155, v182, v157 row_ror:2 row_mask:0xf bank_mask:0xf bound_ctrl:1
	v_mov_b32_dpp v139, v166 row_shr:1 row_mask:0xf bank_mask:0xf bound_ctrl:1
	v_and_b32_dpp v153, v182, v158 row_ror:1 row_mask:0xf bank_mask:0xf bound_ctrl:1
	v_or_b32_sdwa v154, v155, v147 dst_sel:WORD_1 dst_unused:UNUSED_PAD src0_sel:DWORD src1_sel:DWORD
	v_mov_b32_dpp v156, v167 row_shr:1 row_mask:0xf bank_mask:0xf bound_ctrl:1
	v_mov_b32_dpp v171, v167 row_shr:2 row_mask:0xf bank_mask:0xf bound_ctrl:1
	v_and_b32_dpp v187, v183, v158 row_ror:1 row_mask:0xf bank_mask:0xf bound_ctrl:1
	v_and_b32_dpp v183, v183, v157 row_ror:2 row_mask:0xf bank_mask:0xf bound_ctrl:1
	v_mov_b32_dpp v189, v168 row_shr:1 row_mask:0xf bank_mask:0xf bound_ctrl:1
	v_mov_b32_dpp v191, v168 row_shr:2 row_mask:0xf bank_mask:0xf bound_ctrl:1
	v_and_b32_dpp v192, v184, v158 row_ror:1 row_mask:0xf bank_mask:0xf bound_ctrl:1
	v_and_b32_dpp v193, v184, v157 row_ror:2 row_mask:0xf bank_mask:0xf bound_ctrl:1
	v_bitop3_b32 v155, v155, s20, v147 bitop3:0xc8
	v_or_b32_sdwa v146, v153, v139 dst_sel:WORD_1 dst_unused:UNUSED_PAD src0_sel:DWORD src1_sel:DWORD
	v_or_b32_sdwa v170, v187, v156 dst_sel:WORD_1 dst_unused:UNUSED_PAD src0_sel:DWORD src1_sel:DWORD
	v_or_b32_sdwa v182, v183, v171 dst_sel:WORD_1 dst_unused:UNUSED_PAD src0_sel:DWORD src1_sel:DWORD
	v_or_b32_sdwa v186, v192, v189 dst_sel:WORD_1 dst_unused:UNUSED_PAD src0_sel:DWORD src1_sel:DWORD
	v_or_b32_sdwa v184, v193, v191 dst_sel:WORD_1 dst_unused:UNUSED_PAD src0_sel:DWORD src1_sel:DWORD
	v_and_b32_dpp v234, v185, v158 row_ror:1 row_mask:0xf bank_mask:0xf bound_ctrl:1
	v_and_b32_dpp v235, v185, v157 row_ror:2 row_mask:0xf bank_mask:0xf bound_ctrl:1
	v_bitop3_b32 v147, v153, s20, v139 bitop3:0xc8
	v_bitop3_b32 v183, v183, s20, v171 bitop3:0xc8
	v_bitop3_b32 v171, v187, s20, v156 bitop3:0xc8
	v_bitop3_b32 v185, v193, s20, v191 bitop3:0xc8
	v_bitop3_b32 v187, v192, s20, v189 bitop3:0xc8
	s_waitcnt vmcnt(4)
	v_pk_mul_f32 v[192:193], v[110:111], v[138:139] op_sel_hi:[1,0]
	v_pk_mul_f32 v[110:111], v[116:117], v[154:155]
	v_pk_mul_f32 v[114:115], v[114:115], v[138:139] op_sel_hi:[1,0]
	v_pk_fma_f32 v[110:111], v[128:129], v[146:147], v[110:111]
	v_lshlrev_b32_e32 v146, 16, v166
	v_and_b32_e32 v147, 0xffff0000, v166
	v_pk_fma_f32 v[110:111], v[120:121], v[146:147], v[110:111]
	v_pk_mul_f32 v[112:113], v[112:113], v[138:139] op_sel_hi:[1,0]
	v_pk_add_f32 v[110:111], v[124:125], v[110:111]
	v_lshlrev_b32_e32 v154, 16, v167
	v_mul_f32_e32 v139, 0xbfb8aa3b, v110
	v_exp_f32_e32 v146, v139
	v_mul_f32_e32 v139, 0xbfb8aa3b, v111
	v_exp_f32_e32 v147, v139
	v_pk_mul_f32 v[138:139], v[108:109], v[138:139] op_sel_hi:[1,0]
	v_add_f32_e32 v108, 1.0, v146
	v_and_b32_e32 v155, 0xffff0000, v167
	v_add_f32_e32 v109, 1.0, v147
	v_pk_mul_f32 v[146:147], v[118:119], v[182:183]
	v_rcp_f32_e32 v108, v108
	v_pk_fma_f32 v[146:147], v[130:131], v[170:171], v[146:147]
	v_rcp_f32_e32 v109, v109
	v_pk_fma_f32 v[146:147], v[122:123], v[154:155], v[146:147]
	v_mov_b32_dpp v233, v169 row_shr:2 row_mask:0xf bank_mask:0xf bound_ctrl:1
	v_pk_add_f32 v[146:147], v[126:127], v[146:147]
	v_pk_mul_f32 v[108:109], v[110:111], v[108:109]
	v_mul_f32_e32 v153, 0xbfb8aa3b, v146
	v_exp_f32_e32 v153, v153
	v_mul_f32_e32 v154, 0xbfb8aa3b, v147
	v_exp_f32_e32 v155, v154
	v_pk_mul_f32 v[108:109], v[108:109], v[112:113]
	v_add_f32_e32 v153, 1.0, v153
	v_rcp_f32_e32 v154, v153
	v_add_f32_e32 v153, 1.0, v155
	v_rcp_f32_e32 v155, v153
	v_pk_mul_f32 v[112:113], v[44:45], v[184:185]
	v_cvt_pk_bf16_f32 v108, v108, v109
	v_pk_fma_f32 v[112:113], v[48:49], v[186:187], v[112:113]
	v_pk_mul_f32 v[110:111], v[146:147], v[154:155]
	v_mov_b32_dpp v232, v169 row_shr:1 row_mask:0xf bank_mask:0xf bound_ctrl:1
	v_pk_mul_f32 v[110:111], v[110:111], v[114:115]
	v_lshlrev_b32_e32 v114, 16, v168
	v_and_b32_e32 v115, 0xffff0000, v168
	v_pk_fma_f32 v[112:113], v[36:37], v[114:115], v[112:113]
	v_or_b32_sdwa v190, v235, v233 dst_sel:WORD_1 dst_unused:UNUSED_PAD src0_sel:DWORD src1_sel:DWORD
	v_pk_add_f32 v[112:113], v[40:41], v[112:113]
	v_bitop3_b32 v191, v235, s20, v233 bitop3:0xc8
	v_mul_f32_e32 v109, 0xbfb8aa3b, v112
	v_exp_f32_e32 v114, v109
	v_mul_f32_e32 v109, 0xbfb8aa3b, v113
	v_exp_f32_e32 v115, v109
	v_or_b32_sdwa v188, v234, v232 dst_sel:WORD_1 dst_unused:UNUSED_PAD src0_sel:DWORD src1_sel:DWORD
	v_bitop3_b32 v189, v234, s20, v232 bitop3:0xc8
	v_cvt_pk_bf16_f32 v109, v110, v111
	v_add_f32_e32 v110, 1.0, v114
	v_add_f32_e32 v111, 1.0, v115
	v_pk_mul_f32 v[114:115], v[46:47], v[190:191]
	v_lshlrev_b32_e32 v146, 16, v169
	v_pk_fma_f32 v[114:115], v[50:51], v[188:189], v[114:115]
	v_and_b32_e32 v147, 0xffff0000, v169
	v_pk_fma_f32 v[114:115], v[38:39], v[146:147], v[114:115]
	v_rcp_f32_e32 v110, v110
	v_pk_add_f32 v[114:115], v[42:43], v[114:115]
	v_rcp_f32_e32 v111, v111
	v_mul_f32_e32 v146, 0xbfb8aa3b, v114
	v_mul_f32_e32 v147, 0xbfb8aa3b, v115
	v_exp_f32_e32 v146, v146
	v_exp_f32_e32 v147, v147
	v_pk_mul_f32 v[110:111], v[112:113], v[110:111]
	v_add_u32_e32 v156, 0xa0, v220
	v_add_f32_e32 v146, 1.0, v146
	v_add_f32_e32 v147, 1.0, v147
	v_rcp_f32_e32 v146, v146
	v_rcp_f32_e32 v147, v147
	v_pk_mul_f32 v[110:111], v[138:139], v[110:111]
	v_pk_mul_f32 v[112:113], v[114:115], v[146:147]
	s_nop 0
	v_pk_mul_f32 v[112:113], v[192:193], v[112:113]
	v_cvt_pk_bf16_f32 v110, v110, v111
	v_cvt_pk_bf16_f32 v111, v112, v113
	v_mad_i64_i32 v[112:113], s[18:19], v165, s21, v[218:219]
	v_lshl_add_u64 v[138:139], v[112:113], 0, v[206:207]
	global_store_dwordx4 v[138:139], v[108:111], off
	s_waitcnt vmcnt(4)
	v_mov_b32_e32 v112, v230
	v_sub_u32_e32 v113, v159, v1
	v_and_b32_e32 v113, 0xfdf, v113
	v_cmp_ne_u32_e32 vcc, 0, v113
	s_waitcnt vmcnt(1)
	v_mov_b32_dpp v115, v132 row_shr:2 row_mask:0xf bank_mask:0xf bound_ctrl:1
	v_mov_b32_dpp v183, v133 row_shr:1 row_mask:0xf bank_mask:0xf bound_ctrl:1
	v_cndmask_b32_e64 v113, 0, -1, vcc
	v_cndmask_b32_e64 v154, 0, v113, s[38:39]
	v_cndmask_b32_e64 v155, 0, v113, s[36:37]
	v_mov_b32_dpp v113, v132 row_shr:1 row_mask:0xf bank_mask:0xf bound_ctrl:1
	v_and_b32_dpp v147, v166, v154 row_ror:2 row_mask:0xf bank_mask:0xf bound_ctrl:1
	v_and_b32_dpp v153, v166, v155 row_ror:1 row_mask:0xf bank_mask:0xf bound_ctrl:1
	v_or_b32_sdwa v146, v147, v115 dst_sel:WORD_1 dst_unused:UNUSED_PAD src0_sel:DWORD src1_sel:DWORD
	v_mov_b32_dpp v171, v133 row_shr:2 row_mask:0xf bank_mask:0xf bound_ctrl:1
	v_and_b32_dpp v185, v167, v155 row_ror:1 row_mask:0xf bank_mask:0xf bound_ctrl:1
	v_and_b32_dpp v167, v167, v154 row_ror:2 row_mask:0xf bank_mask:0xf bound_ctrl:1
	v_mov_b32_dpp v187, v134 row_shr:1 row_mask:0xf bank_mask:0xf bound_ctrl:1
	v_mov_b32_dpp v188, v134 row_shr:2 row_mask:0xf bank_mask:0xf bound_ctrl:1
	v_and_b32_dpp v189, v168, v155 row_ror:1 row_mask:0xf bank_mask:0xf bound_ctrl:1
	v_and_b32_dpp v190, v168, v154 row_ror:2 row_mask:0xf bank_mask:0xf bound_ctrl:1
	v_bitop3_b32 v147, v147, s20, v115 bitop3:0xc8
	v_or_b32_sdwa v114, v153, v113 dst_sel:WORD_1 dst_unused:UNUSED_PAD src0_sel:DWORD src1_sel:DWORD
	v_or_b32_sdwa v166, v185, v183 dst_sel:WORD_1 dst_unused:UNUSED_PAD src0_sel:DWORD src1_sel:DWORD
	v_or_b32_sdwa v170, v167, v171 dst_sel:WORD_1 dst_unused:UNUSED_PAD src0_sel:DWORD src1_sel:DWORD
	v_or_b32_sdwa v182, v189, v187 dst_sel:WORD_1 dst_unused:UNUSED_PAD src0_sel:DWORD src1_sel:DWORD
	v_or_b32_sdwa v168, v190, v188 dst_sel:WORD_1 dst_unused:UNUSED_PAD src0_sel:DWORD src1_sel:DWORD
	v_and_b32_dpp v193, v169, v155 row_ror:1 row_mask:0xf bank_mask:0xf bound_ctrl:1
	v_and_b32_dpp v232, v169, v154 row_ror:2 row_mask:0xf bank_mask:0xf bound_ctrl:1
	v_bitop3_b32 v115, v153, s20, v113 bitop3:0xc8
	v_bitop3_b32 v171, v167, s20, v171 bitop3:0xc8
	v_bitop3_b32 v167, v185, s20, v183 bitop3:0xc8
	v_bitop3_b32 v169, v190, s20, v188 bitop3:0xc8
	v_bitop3_b32 v183, v189, s20, v187 bitop3:0xc8
	v_mov_b32_dpp v192, v135 row_shr:2 row_mask:0xf bank_mask:0xf bound_ctrl:1
	v_mov_b32_dpp v191, v135 row_shr:1 row_mask:0xf bank_mask:0xf bound_ctrl:1
	v_or_b32_sdwa v186, v232, v192 dst_sel:WORD_1 dst_unused:UNUSED_PAD src0_sel:DWORD src1_sel:DWORD
	v_bitop3_b32 v187, v232, s20, v192 bitop3:0xc8
	v_or_b32_sdwa v184, v193, v191 dst_sel:WORD_1 dst_unused:UNUSED_PAD src0_sel:DWORD src1_sel:DWORD
	v_bitop3_b32 v185, v193, s20, v191 bitop3:0xc8
	v_mad_i64_i32 v[108:109], s[18:19], v156, s21, v[224:225]
	global_load_dwordx4 v[108:111], v[108:109], off
	v_add_u32_e32 v251, 16, v156
	v_mad_i64_i32 v[226:227], s[100:101], v251, s21, v[224:225]
	global_load_dwordx4 v[226:229], v[226:227], off
	v_add_u32_e32 v153, 0xb0, v220
	s_waitcnt lgkmcnt(0)
	v_pk_mul_f32 v[188:189], v[102:103], v[112:113] op_sel_hi:[1,0]
	v_pk_mul_f32 v[102:103], v[116:117], v[146:147]
	v_pk_mul_f32 v[106:107], v[106:107], v[112:113] op_sel_hi:[1,0]
	v_pk_fma_f32 v[102:103], v[128:129], v[114:115], v[102:103]
	v_lshlrev_b32_e32 v114, 16, v132
	v_and_b32_e32 v115, 0xffff0000, v132
	v_pk_fma_f32 v[102:103], v[120:121], v[114:115], v[102:103]
	v_pk_mul_f32 v[104:105], v[104:105], v[112:113] op_sel_hi:[1,0]
	v_pk_add_f32 v[102:103], v[124:125], v[102:103]
	v_lshlrev_b32_e32 v146, 16, v133
	v_mul_f32_e32 v113, 0xbfb8aa3b, v102
	v_exp_f32_e32 v114, v113
	v_mul_f32_e32 v113, 0xbfb8aa3b, v103
	v_exp_f32_e32 v115, v113
	v_pk_mul_f32 v[112:113], v[100:101], v[112:113] op_sel_hi:[1,0]
	v_add_f32_e32 v100, 1.0, v114
	v_and_b32_e32 v147, 0xffff0000, v133
	v_add_f32_e32 v101, 1.0, v115
	v_pk_mul_f32 v[114:115], v[118:119], v[170:171]
	v_rcp_f32_e32 v100, v100
	v_pk_fma_f32 v[114:115], v[130:131], v[166:167], v[114:115]
	v_rcp_f32_e32 v101, v101
	v_pk_fma_f32 v[114:115], v[122:123], v[146:147], v[114:115]
	v_pk_mul_f32 v[100:101], v[102:103], v[100:101]
	v_pk_add_f32 v[114:115], v[126:127], v[114:115]
	v_pk_mul_f32 v[100:101], v[100:101], v[104:105]
	v_mul_f32_e32 v146, 0xbfb8aa3b, v114
	v_mul_f32_e32 v147, 0xbfb8aa3b, v115
	v_exp_f32_e32 v146, v146
	v_exp_f32_e32 v147, v147
	v_pk_mul_f32 v[104:105], v[44:45], v[168:169]
	v_cvt_pk_bf16_f32 v100, v100, v101
	v_add_f32_e32 v146, 1.0, v146
	v_add_f32_e32 v147, 1.0, v147
	v_rcp_f32_e32 v146, v146
	v_rcp_f32_e32 v147, v147
	v_pk_fma_f32 v[104:105], v[48:49], v[182:183], v[104:105]
	v_pk_mul_f32 v[102:103], v[114:115], v[146:147]
	s_nop 0
	v_pk_mul_f32 v[102:103], v[102:103], v[106:107]
	v_lshlrev_b32_e32 v106, 16, v134
	v_and_b32_e32 v107, 0xffff0000, v134
	v_pk_fma_f32 v[104:105], v[36:37], v[106:107], v[104:105]
	v_lshlrev_b32_e32 v114, 16, v135
	v_pk_add_f32 v[104:105], v[40:41], v[104:105]
	v_and_b32_e32 v115, 0xffff0000, v135
	v_mul_f32_e32 v101, 0xbfb8aa3b, v104
	v_exp_f32_e32 v106, v101
	v_mul_f32_e32 v101, 0xbfb8aa3b, v105
	v_exp_f32_e32 v107, v101
	v_cvt_pk_bf16_f32 v101, v102, v103
	v_add_f32_e32 v102, 1.0, v106
	v_rcp_f32_e32 v102, v102
	v_add_f32_e32 v103, 1.0, v107
	v_pk_mul_f32 v[106:107], v[46:47], v[186:187]
	v_rcp_f32_e32 v103, v103
	v_pk_fma_f32 v[106:107], v[50:51], v[184:185], v[106:107]
	v_pk_mul_f32 v[102:103], v[104:105], v[102:103]
	v_pk_fma_f32 v[106:107], v[38:39], v[114:115], v[106:107]
	v_pk_mul_f32 v[102:103], v[112:113], v[102:103]
	v_pk_add_f32 v[106:107], v[42:43], v[106:107]
	v_cvt_pk_bf16_f32 v102, v102, v103
	v_mul_f32_e32 v114, 0xbfb8aa3b, v106
	v_mul_f32_e32 v115, 0xbfb8aa3b, v107
	v_exp_f32_e32 v114, v114
	v_exp_f32_e32 v115, v115
	v_add_f32_e32 v114, 1.0, v114
	v_add_f32_e32 v115, 1.0, v115
	v_rcp_f32_e32 v114, v114
	v_rcp_f32_e32 v115, v115
	s_nop 0
	v_pk_mul_f32 v[104:105], v[106:107], v[114:115]
	s_nop 0
	v_pk_mul_f32 v[104:105], v[188:189], v[104:105]
	s_nop 0
	v_cvt_pk_bf16_f32 v103, v104, v105
	v_mad_i64_i32 v[104:105], s[18:19], v159, s21, v[218:219]
	v_lshl_add_u64 v[114:115], v[104:105], 0, v[206:207]
	global_store_dwordx4 v[114:115], v[100:103], off
	s_nop 1
	v_mov_b32_e32 v100, v231
	s_nop 0
	v_sub_u32_e32 v101, v156, v1
	v_and_b32_e32 v101, 0xfff, v101
	v_cmp_ne_u32_e32 vcc, 0, v101
	v_mad_i64_i32 v[102:103], s[18:19], v153, s21, v[224:225]
	s_nop 0
	v_cndmask_b32_e64 v101, 0, -1, vcc
	v_cndmask_b32_e64 v146, 0, v101, s[38:39]
	s_waitcnt vmcnt(1)
	v_mov_b32_e32 v102, v226
	v_mov_b32_e32 v103, v227
	v_mov_b32_e32 v104, v228
	v_mov_b32_e32 v105, v229
	s_nop 1
	v_cndmask_b32_e64 v147, 0, v101, s[36:37]
	v_mov_b32_dpp v107, v108 row_shr:2 row_mask:0xf bank_mask:0xf bound_ctrl:1
	v_and_b32_dpp v113, v132, v146 row_ror:2 row_mask:0xf bank_mask:0xf bound_ctrl:1
	v_mov_b32_dpp v101, v108 row_shr:1 row_mask:0xf bank_mask:0xf bound_ctrl:1
	v_and_b32_dpp v167, v132, v147 row_ror:1 row_mask:0xf bank_mask:0xf bound_ctrl:1
	v_or_b32_sdwa v112, v113, v107 dst_sel:WORD_1 dst_unused:UNUSED_PAD src0_sel:DWORD src1_sel:DWORD
	v_mov_b32_dpp v169, v109 row_shr:1 row_mask:0xf bank_mask:0xf bound_ctrl:1
	v_mov_b32_dpp v171, v109 row_shr:2 row_mask:0xf bank_mask:0xf bound_ctrl:1
	v_and_b32_dpp v183, v133, v147 row_ror:1 row_mask:0xf bank_mask:0xf bound_ctrl:1
	v_and_b32_dpp v133, v133, v146 row_ror:2 row_mask:0xf bank_mask:0xf bound_ctrl:1
	v_mov_b32_dpp v184, v110 row_shr:1 row_mask:0xf bank_mask:0xf bound_ctrl:1
	v_mov_b32_dpp v185, v110 row_shr:2 row_mask:0xf bank_mask:0xf bound_ctrl:1
	v_and_b32_dpp v186, v134, v147 row_ror:1 row_mask:0xf bank_mask:0xf bound_ctrl:1
	v_and_b32_dpp v187, v134, v146 row_ror:2 row_mask:0xf bank_mask:0xf bound_ctrl:1
	v_bitop3_b32 v113, v113, s20, v107 bitop3:0xc8
	v_or_b32_sdwa v106, v167, v101 dst_sel:WORD_1 dst_unused:UNUSED_PAD src0_sel:DWORD src1_sel:DWORD
	v_or_b32_sdwa v132, v183, v169 dst_sel:WORD_1 dst_unused:UNUSED_PAD src0_sel:DWORD src1_sel:DWORD
	v_or_b32_sdwa v166, v133, v171 dst_sel:WORD_1 dst_unused:UNUSED_PAD src0_sel:DWORD src1_sel:DWORD
	v_or_b32_sdwa v168, v186, v184 dst_sel:WORD_1 dst_unused:UNUSED_PAD src0_sel:DWORD src1_sel:DWORD
	v_or_b32_sdwa v134, v187, v185 dst_sel:WORD_1 dst_unused:UNUSED_PAD src0_sel:DWORD src1_sel:DWORD
	v_and_b32_dpp v190, v135, v147 row_ror:1 row_mask:0xf bank_mask:0xf bound_ctrl:1
	v_and_b32_dpp v191, v135, v146 row_ror:2 row_mask:0xf bank_mask:0xf bound_ctrl:1
	v_bitop3_b32 v107, v167, s20, v101 bitop3:0xc8
	v_bitop3_b32 v167, v133, s20, v171 bitop3:0xc8
	v_bitop3_b32 v133, v183, s20, v169 bitop3:0xc8
	v_bitop3_b32 v135, v187, s20, v185 bitop3:0xc8
	v_bitop3_b32 v169, v186, s20, v184 bitop3:0xc8
	v_mov_b32_dpp v189, v111 row_shr:2 row_mask:0xf bank_mask:0xf bound_ctrl:1
	v_mov_b32_dpp v188, v111 row_shr:1 row_mask:0xf bank_mask:0xf bound_ctrl:1
	v_or_b32_sdwa v182, v191, v189 dst_sel:WORD_1 dst_unused:UNUSED_PAD src0_sel:DWORD src1_sel:DWORD
	v_bitop3_b32 v183, v191, s20, v189 bitop3:0xc8
	v_or_b32_sdwa v170, v190, v188 dst_sel:WORD_1 dst_unused:UNUSED_PAD src0_sel:DWORD src1_sel:DWORD
	v_bitop3_b32 v171, v190, s20, v188 bitop3:0xc8
	s_andn2_b64 vcc, exec, s[40:41]
	s_waitcnt lgkmcnt(0)
	v_pk_mul_f32 v[184:185], v[62:63], v[100:101] op_sel_hi:[1,0]
	v_pk_mul_f32 v[62:63], v[116:117], v[112:113]
	v_pk_mul_f32 v[66:67], v[66:67], v[100:101] op_sel_hi:[1,0]
	v_pk_fma_f32 v[62:63], v[128:129], v[106:107], v[62:63]
	v_lshlrev_b32_e32 v106, 16, v108
	v_and_b32_e32 v107, 0xffff0000, v108
	v_pk_fma_f32 v[62:63], v[120:121], v[106:107], v[62:63]
	v_pk_mul_f32 v[64:65], v[64:65], v[100:101] op_sel_hi:[1,0]
	v_pk_add_f32 v[62:63], v[124:125], v[62:63]
	v_lshlrev_b32_e32 v112, 16, v109
	v_mul_f32_e32 v101, 0xbfb8aa3b, v62
	v_exp_f32_e32 v106, v101
	v_mul_f32_e32 v101, 0xbfb8aa3b, v63
	v_exp_f32_e32 v107, v101
	v_pk_mul_f32 v[100:101], v[60:61], v[100:101] op_sel_hi:[1,0]
	v_add_f32_e32 v60, 1.0, v106
	v_and_b32_e32 v113, 0xffff0000, v109
	v_add_f32_e32 v61, 1.0, v107
	v_pk_mul_f32 v[106:107], v[118:119], v[166:167]
	v_rcp_f32_e32 v60, v60
	v_pk_fma_f32 v[106:107], v[130:131], v[132:133], v[106:107]
	v_rcp_f32_e32 v61, v61
	v_pk_fma_f32 v[106:107], v[122:123], v[112:113], v[106:107]
	v_mov_b32_dpp v133, v103 row_shr:2 row_mask:0xf bank_mask:0xf bound_ctrl:1
	v_pk_add_f32 v[106:107], v[126:127], v[106:107]
	v_pk_mul_f32 v[60:61], v[62:63], v[60:61]
	v_mul_f32_e32 v112, 0xbfb8aa3b, v106
	v_mul_f32_e32 v113, 0xbfb8aa3b, v107
	v_exp_f32_e32 v112, v112
	v_exp_f32_e32 v113, v113
	v_pk_mul_f32 v[60:61], v[60:61], v[64:65]
	v_pk_mul_f32 v[64:65], v[44:45], v[134:135]
	v_add_f32_e32 v112, 1.0, v112
	v_add_f32_e32 v113, 1.0, v113
	v_rcp_f32_e32 v112, v112
	v_rcp_f32_e32 v113, v113
	v_pk_fma_f32 v[64:65], v[48:49], v[168:169], v[64:65]
	v_cvt_pk_bf16_f32 v60, v60, v61
	v_mov_b32_dpp v135, v104 row_shr:1 row_mask:0xf bank_mask:0xf bound_ctrl:1
	v_pk_mul_f32 v[62:63], v[106:107], v[112:113]
	v_lshlrev_b32_e32 v106, 16, v111
	v_pk_mul_f32 v[62:63], v[62:63], v[66:67]
	v_lshlrev_b32_e32 v66, 16, v110
	v_and_b32_e32 v67, 0xffff0000, v110
	v_pk_fma_f32 v[64:65], v[36:37], v[66:67], v[64:65]
	v_and_b32_e32 v107, 0xffff0000, v111
	v_pk_add_f32 v[64:65], v[40:41], v[64:65]
	v_mov_b32_dpp v166, v104 row_shr:2 row_mask:0xf bank_mask:0xf bound_ctrl:1
	v_mul_f32_e32 v61, 0xbfb8aa3b, v64
	v_exp_f32_e32 v66, v61
	v_mul_f32_e32 v61, 0xbfb8aa3b, v65
	v_exp_f32_e32 v67, v61
	v_cvt_pk_bf16_f32 v61, v62, v63
	v_add_f32_e32 v62, 1.0, v66
	v_rcp_f32_e32 v62, v62
	v_add_f32_e32 v63, 1.0, v67
	v_pk_mul_f32 v[66:67], v[46:47], v[182:183]
	v_rcp_f32_e32 v63, v63
	v_pk_fma_f32 v[66:67], v[50:51], v[170:171], v[66:67]
	v_mov_b32_dpp v170, v105 row_shr:2 row_mask:0xf bank_mask:0xf bound_ctrl:1
	v_pk_fma_f32 v[66:67], v[38:39], v[106:107], v[66:67]
	v_pk_mul_f32 v[62:63], v[64:65], v[62:63]
	v_pk_add_f32 v[66:67], v[42:43], v[66:67]
	v_pk_mul_f32 v[62:63], v[100:101], v[62:63]
	v_mul_f32_e32 v106, 0xbfb8aa3b, v66
	v_mul_f32_e32 v107, 0xbfb8aa3b, v67
	v_exp_f32_e32 v106, v106
	v_exp_f32_e32 v107, v107
	v_cvt_pk_bf16_f32 v62, v62, v63
	v_mov_b32_dpp v169, v105 row_shr:1 row_mask:0xf bank_mask:0xf bound_ctrl:1
	v_add_f32_e32 v106, 1.0, v106
	v_add_f32_e32 v107, 1.0, v107
	v_rcp_f32_e32 v106, v106
	v_rcp_f32_e32 v107, v107
	s_nop 0
	v_pk_mul_f32 v[64:65], v[66:67], v[106:107]
	s_nop 0
	v_pk_mul_f32 v[64:65], v[184:185], v[64:65]
	v_mov_b32_dpp v107, v103 row_shr:1 row_mask:0xf bank_mask:0xf bound_ctrl:1
	v_cvt_pk_bf16_f32 v63, v64, v65
	v_mad_i64_i32 v[64:65], s[18:19], v156, s21, v[218:219]
	v_lshl_add_u64 v[112:113], v[64:65], 0, v[206:207]
	global_store_dwordx4 v[112:113], v[60:63], off
	v_mov_b32_e32 v64, v240
	s_nop 0
	v_mov_b32_dpp v60, v108 row_ror:1 row_mask:0xf bank_mask:0xf bound_ctrl:1
	v_mov_b32_dpp v62, v108 row_ror:2 row_mask:0xf bank_mask:0xf bound_ctrl:1
	v_cndmask_b32_e64 v65, 0, v60, s[36:37]
	v_mov_b32_dpp v60, v109 row_ror:1 row_mask:0xf bank_mask:0xf bound_ctrl:1
	v_mov_b32_dpp v63, v102 row_shr:2 row_mask:0xf bank_mask:0xf bound_ctrl:1
	v_cndmask_b32_e64 v67, 0, v62, s[38:39]
	v_mov_b32_dpp v62, v109 row_ror:2 row_mask:0xf bank_mask:0xf bound_ctrl:1
	v_cndmask_b32_e64 v134, 0, v60, s[36:37]
	v_mov_b32_dpp v60, v110 row_ror:1 row_mask:0xf bank_mask:0xf bound_ctrl:1
	v_mov_b32_dpp v61, v102 row_shr:1 row_mask:0xf bank_mask:0xf bound_ctrl:1
	v_or_b32_sdwa v100, v67, v63 dst_sel:WORD_1 dst_unused:UNUSED_PAD src0_sel:DWORD src1_sel:DWORD
	v_cndmask_b32_e64 v109, 0, v62, s[38:39]
	v_mov_b32_dpp v62, v110 row_ror:2 row_mask:0xf bank_mask:0xf bound_ctrl:1
	v_cndmask_b32_e64 v167, 0, v60, s[36:37]
	v_bitop3_b32 v101, v67, s20, v63 bitop3:0xc8
	v_or_b32_sdwa v66, v65, v61 dst_sel:WORD_1 dst_unused:UNUSED_PAD src0_sel:DWORD src1_sel:DWORD
	v_or_b32_sdwa v106, v134, v107 dst_sel:WORD_1 dst_unused:UNUSED_PAD src0_sel:DWORD src1_sel:DWORD
	v_or_b32_sdwa v110, v167, v135 dst_sel:WORD_1 dst_unused:UNUSED_PAD src0_sel:DWORD src1_sel:DWORD
	v_cndmask_b32_e64 v168, 0, v62, s[38:39]
	v_mov_b32_dpp v60, v111 row_ror:1 row_mask:0xf bank_mask:0xf bound_ctrl:1
	v_mov_b32_dpp v62, v111 row_ror:2 row_mask:0xf bank_mask:0xf bound_ctrl:1
	v_bitop3_b32 v67, v65, s20, v61 bitop3:0xc8
	v_bitop3_b32 v107, v134, s20, v107 bitop3:0xc8
	v_bitop3_b32 v111, v167, s20, v135 bitop3:0xc8
	v_or_b32_sdwa v108, v109, v133 dst_sel:WORD_1 dst_unused:UNUSED_PAD src0_sel:DWORD src1_sel:DWORD
	v_bitop3_b32 v109, v109, s20, v133 bitop3:0xc8
	v_or_b32_sdwa v132, v168, v166 dst_sel:WORD_1 dst_unused:UNUSED_PAD src0_sel:DWORD src1_sel:DWORD
	v_bitop3_b32 v133, v168, s20, v166 bitop3:0xc8
	v_pk_mul_f32 v[44:45], v[44:45], v[132:133]
	v_cndmask_b32_e64 v182, 0, v62, s[38:39]
	v_pk_fma_f32 v[44:45], v[48:49], v[110:111], v[44:45]
	v_lshlrev_b32_e32 v48, 16, v104
	v_and_b32_e32 v49, 0xffff0000, v104
	v_pk_fma_f32 v[36:37], v[36:37], v[48:49], v[44:45]
	v_cndmask_b32_e64 v171, 0, v60, s[36:37]
	v_pk_add_f32 v[40:41], v[40:41], v[36:37]
	v_or_b32_sdwa v62, v182, v170 dst_sel:WORD_1 dst_unused:UNUSED_PAD src0_sel:DWORD src1_sel:DWORD
	v_mul_f32_e32 v36, 0xbfb8aa3b, v40
	v_exp_f32_e32 v44, v36
	v_or_b32_e32 v36, 0x80, v222
	v_ashrrev_i32_e32 v37, 31, v36
	v_bitop3_b32 v63, v182, s20, v170 bitop3:0xc8
	v_mad_i64_i32 v[48:49], s[18:19], v220, s21, v[204:205]
	v_or_b32_sdwa v60, v171, v169 dst_sel:WORD_1 dst_unused:UNUSED_PAD src0_sel:DWORD src1_sel:DWORD
	v_bitop3_b32 v61, v171, s20, v169 bitop3:0xc8
	v_pk_mul_f32 v[46:47], v[46:47], v[62:63]
	v_mul_f32_e32 v45, 0xbfb8aa3b, v41
	v_pk_fma_f32 v[46:47], v[50:51], v[60:61], v[46:47]
	v_exp_f32_e32 v45, v45
	v_add_f32_e32 v44, 1.0, v44
	v_rcp_f32_e32 v44, v44
	v_add_f32_e32 v45, 1.0, v45
	v_rcp_f32_e32 v45, v45
	s_waitcnt lgkmcnt(0)
	v_pk_mul_f32 v[134:135], v[56:57], v[64:65] op_sel_hi:[1,0]
	v_pk_mul_f32 v[56:57], v[54:55], v[64:65] op_sel_hi:[1,0]
	v_pk_mul_f32 v[54:55], v[116:117], v[100:101]
	v_pk_mul_f32 v[58:59], v[58:59], v[64:65] op_sel_hi:[1,0]
	v_pk_fma_f32 v[54:55], v[128:129], v[66:67], v[54:55]
	v_lshlrev_b32_e32 v66, 16, v102
	v_and_b32_e32 v67, 0xffff0000, v102
	v_pk_fma_f32 v[54:55], v[120:121], v[66:67], v[54:55]
	v_and_b32_e32 v101, 0xffff0000, v103
	v_pk_add_f32 v[66:67], v[124:125], v[54:55]
	v_pk_mul_f32 v[40:41], v[40:41], v[44:45]
	v_mul_f32_e32 v54, 0xbfb8aa3b, v66
	v_exp_f32_e32 v65, v54
	v_mul_f32_e32 v54, 0xbfb8aa3b, v67
	v_exp_f32_e32 v100, v54
	v_pk_mul_f32 v[54:55], v[52:53], v[64:65] op_sel_hi:[1,0]
	v_add_f32_e32 v52, 1.0, v65
	v_pk_mul_f32 v[64:65], v[118:119], v[108:109]
	v_add_f32_e32 v53, 1.0, v100
	v_pk_fma_f32 v[64:65], v[130:131], v[106:107], v[64:65]
	v_lshlrev_b32_e32 v100, 16, v103
	v_pk_fma_f32 v[64:65], v[122:123], v[100:101], v[64:65]
	v_lshlrev_b64 v[108:109], 1, v[36:37]
	v_pk_add_f32 v[64:65], v[126:127], v[64:65]
	v_lshl_add_u64 v[48:49], v[48:49], 0, v[108:109]
	v_mul_f32_e32 v100, 0xbfb8aa3b, v64
	v_mul_f32_e32 v101, 0xbfb8aa3b, v65
	v_exp_f32_e32 v100, v100
	v_exp_f32_e32 v101, v101
	global_load_dwordx4 v[116:119], v[216:217], off offset:256
	v_rcp_f32_e32 v52, v52
	v_add_f32_e32 v100, 1.0, v100
	v_add_f32_e32 v101, 1.0, v101
	v_rcp_f32_e32 v100, v100
	v_rcp_f32_e32 v101, v101
	v_rcp_f32_e32 v53, v53
	v_pk_mul_f32 v[40:41], v[54:55], v[40:41]
	v_lshlrev_b64 v[36:37], 2, v[36:37]
	v_pk_mul_f32 v[64:65], v[64:65], v[100:101]
	global_load_dwordx4 v[100:103], v[48:49], off
	v_lshlrev_b32_e32 v48, 16, v105
	v_and_b32_e32 v49, 0xffff0000, v105
	v_pk_fma_f32 v[38:39], v[38:39], v[48:49], v[46:47]
	v_pk_mul_f32 v[52:53], v[66:67], v[52:53]
	v_pk_add_f32 v[38:39], v[42:43], v[38:39]
	v_pk_mul_f32 v[52:53], v[52:53], v[134:135]
	v_mul_f32_e32 v42, 0xbfb8aa3b, v38
	v_mul_f32_e32 v43, 0xbfb8aa3b, v39
	v_exp_f32_e32 v42, v42
	v_exp_f32_e32 v43, v43
	v_pk_mul_f32 v[58:59], v[64:65], v[58:59]
	v_cvt_pk_bf16_f32 v52, v52, v53
	v_add_f32_e32 v42, 1.0, v42
	v_add_f32_e32 v43, 1.0, v43
	v_rcp_f32_e32 v42, v42
	v_rcp_f32_e32 v43, v43
	v_cvt_pk_bf16_f32 v53, v58, v59
	v_cvt_pk_bf16_f32 v54, v40, v41
	v_mad_i64_i32 v[104:105], s[18:19], v212, s21, v[204:205]
	v_pk_mul_f32 v[38:39], v[38:39], v[42:43]
	v_lshl_add_u64 v[104:105], v[104:105], 0, v[108:109]
	v_pk_mul_f32 v[38:39], v[56:57], v[38:39]
	s_waitcnt lgkmcnt(0)
	s_waitcnt vmcnt(1)
	v_and_b32_dpp v127, v116, v223 row_ror:2 row_mask:0xf bank_mask:0xf bound_ctrl:1
	v_cvt_pk_bf16_f32 v55, v38, v39
	v_mad_i64_i32 v[38:39], s[18:19], v153, s21, v[218:219]
	v_lshl_add_u64 v[110:111], v[38:39], 0, v[206:207]
	global_store_dwordx4 v[110:111], v[52:55], off
	global_load_dword v120, v[202:203], off
	global_load_dword v230, v[202:203], off offset:64
	global_load_dword v231, v[202:203], off offset:128
	global_load_dword v240, v[202:203], off offset:192
	v_lshl_add_u64 v[38:39], v[194:195], 0, v[36:37]
	global_load_dwordx4 v[64:67], v[208:209], off offset:512
	global_load_dwordx4 v[60:63], v[38:39], off
	v_lshl_add_u64 v[36:37], v[196:197], 0, v[36:37]
	global_load_dwordx4 v[52:55], v[36:37], off
	global_load_dwordx4 v[56:59], v[210:211], off offset:512
	global_load_dwordx4 v[48:51], v[208:209], off offset:528
	global_load_dwordx4 v[44:47], v[38:39], off offset:16
	s_nop 0
	global_load_dwordx4 v[36:39], v[36:37], off offset:16
	s_nop 0
	global_load_dwordx4 v[40:43], v[210:211], off offset:528
	s_waitcnt vmcnt(13)
	v_mov_b32_dpp v123, v100 row_shr:2 row_mask:0xf bank_mask:0xf bound_ctrl:1
	v_mov_b32_dpp v121, v100 row_shr:1 row_mask:0xf bank_mask:0xf bound_ctrl:1
	v_and_b32_dpp v125, v116, v245 row_ror:1 row_mask:0xf bank_mask:0xf bound_ctrl:1
	v_or_b32_sdwa v116, v127, v123 dst_sel:WORD_1 dst_unused:UNUSED_PAD src0_sel:DWORD src1_sel:DWORD
	v_mov_b32_dpp v129, v101 row_shr:1 row_mask:0xf bank_mask:0xf bound_ctrl:1
	v_mov_b32_dpp v131, v101 row_shr:2 row_mask:0xf bank_mask:0xf bound_ctrl:1
	v_and_b32_dpp v133, v117, v245 row_ror:1 row_mask:0xf bank_mask:0xf bound_ctrl:1
	v_and_b32_dpp v134, v117, v223 row_ror:2 row_mask:0xf bank_mask:0xf bound_ctrl:1
	v_mov_b32_dpp v135, v102 row_shr:1 row_mask:0xf bank_mask:0xf bound_ctrl:1
	v_and_b32_dpp v167, v118, v245 row_ror:1 row_mask:0xf bank_mask:0xf bound_ctrl:1
	v_bitop3_b32 v117, v127, s20, v123 bitop3:0xc8
	v_or_b32_sdwa v122, v125, v121 dst_sel:WORD_1 dst_unused:UNUSED_PAD src0_sel:DWORD src1_sel:DWORD
	v_or_b32_sdwa v124, v133, v129 dst_sel:WORD_1 dst_unused:UNUSED_PAD src0_sel:DWORD src1_sel:DWORD
	v_or_b32_sdwa v126, v134, v131 dst_sel:WORD_1 dst_unused:UNUSED_PAD src0_sel:DWORD src1_sel:DWORD
	v_or_b32_sdwa v128, v167, v135 dst_sel:WORD_1 dst_unused:UNUSED_PAD src0_sel:DWORD src1_sel:DWORD
	v_bitop3_b32 v123, v125, s20, v121 bitop3:0xc8
	v_bitop3_b32 v127, v134, s20, v131 bitop3:0xc8
	v_bitop3_b32 v125, v133, s20, v129 bitop3:0xc8
	v_bitop3_b32 v129, v167, s20, v135 bitop3:0xc8
	v_mov_b32_dpp v166, v102 row_shr:2 row_mask:0xf bank_mask:0xf bound_ctrl:1
	v_and_b32_dpp v168, v118, v223 row_ror:2 row_mask:0xf bank_mask:0xf bound_ctrl:1
	v_or_b32_sdwa v118, v168, v166 dst_sel:WORD_1 dst_unused:UNUSED_PAD src0_sel:DWORD src1_sel:DWORD
	v_and_b32_dpp v171, v119, v245 row_ror:1 row_mask:0xf bank_mask:0xf bound_ctrl:1
	v_and_b32_dpp v182, v119, v223 row_ror:2 row_mask:0xf bank_mask:0xf bound_ctrl:1
	v_bitop3_b32 v119, v168, s20, v166 bitop3:0xc8
	v_mov_b32_dpp v170, v103 row_shr:2 row_mask:0xf bank_mask:0xf bound_ctrl:1
	v_mov_b32_dpp v169, v103 row_shr:1 row_mask:0xf bank_mask:0xf bound_ctrl:1
	v_or_b32_sdwa v132, v182, v170 dst_sel:WORD_1 dst_unused:UNUSED_PAD src0_sel:DWORD src1_sel:DWORD
	v_bitop3_b32 v133, v182, s20, v170 bitop3:0xc8
	v_or_b32_sdwa v130, v171, v169 dst_sel:WORD_1 dst_unused:UNUSED_PAD src0_sel:DWORD src1_sel:DWORD
	v_bitop3_b32 v131, v171, s20, v169 bitop3:0xc8
	global_load_dwordx4 v[104:107], v[104:105], off
	s_waitcnt lgkmcnt(0)
	s_waitcnt vmcnt(12)
	v_pk_mul_f32 v[134:135], v[94:95], v[120:121] op_sel_hi:[1,0]
	s_waitcnt vmcnt(8)
	v_pk_mul_f32 v[94:95], v[64:65], v[116:117]
	v_lshlrev_b32_e32 v116, 16, v100
	s_waitcnt vmcnt(7)
	v_pk_fma_f32 v[94:95], v[60:61], v[122:123], v[94:95]
	v_and_b32_e32 v117, 0xffff0000, v100
	s_waitcnt vmcnt(6)
	v_pk_fma_f32 v[94:95], v[52:53], v[116:117], v[94:95]
	v_pk_mul_f32 v[98:99], v[98:99], v[120:121] op_sel_hi:[1,0]
	s_waitcnt vmcnt(5)
	v_pk_add_f32 v[94:95], v[56:57], v[94:95]
	v_pk_mul_f32 v[96:97], v[96:97], v[120:121] op_sel_hi:[1,0]
	v_mul_f32_e32 v116, 0xbfb8aa3b, v94
	v_exp_f32_e32 v121, v116
	v_mul_f32_e32 v116, 0xbfb8aa3b, v95
	v_exp_f32_e32 v122, v116
	v_and_b32_e32 v123, 0xffff0000, v101
	v_pk_mul_f32 v[116:117], v[92:93], v[120:121] op_sel_hi:[1,0]
	v_add_f32_e32 v92, 1.0, v121
	v_pk_mul_f32 v[120:121], v[66:67], v[126:127]
	v_add_f32_e32 v93, 1.0, v122
	v_pk_fma_f32 v[120:121], v[62:63], v[124:125], v[120:121]
	v_lshlrev_b32_e32 v122, 16, v101
	v_pk_fma_f32 v[120:121], v[54:55], v[122:123], v[120:121]
	v_rcp_f32_e32 v92, v92
	v_pk_add_f32 v[120:121], v[58:59], v[120:121]
	v_rcp_f32_e32 v93, v93
	v_mul_f32_e32 v122, 0xbfb8aa3b, v120
	v_mul_f32_e32 v123, 0xbfb8aa3b, v121
	v_exp_f32_e32 v122, v122
	v_exp_f32_e32 v123, v123
	v_pk_mul_f32 v[92:93], v[94:95], v[92:93]
	v_and_b32_dpp v125, v101, v221 row_ror:1 row_mask:0xf bank_mask:0xf bound_ctrl:1
	v_add_f32_e32 v122, 1.0, v122
	v_add_f32_e32 v123, 1.0, v123
	v_rcp_f32_e32 v122, v122
	v_rcp_f32_e32 v123, v123
	v_pk_mul_f32 v[92:93], v[92:93], v[96:97]
	s_waitcnt vmcnt(4)
	v_pk_mul_f32 v[96:97], v[48:49], v[118:119]
	v_cvt_pk_bf16_f32 v92, v92, v93
	v_pk_mul_f32 v[94:95], v[120:121], v[122:123]
	s_waitcnt vmcnt(3)
	v_pk_fma_f32 v[96:97], v[44:45], v[128:129], v[96:97]
	v_pk_mul_f32 v[94:95], v[98:99], v[94:95]
	v_lshlrev_b32_e32 v98, 16, v102
	v_and_b32_e32 v99, 0xffff0000, v102
	s_waitcnt vmcnt(2)
	v_pk_fma_f32 v[96:97], v[36:37], v[98:99], v[96:97]
	v_lshlrev_b32_e32 v118, 16, v103
	s_waitcnt vmcnt(1)
	v_pk_add_f32 v[96:97], v[40:41], v[96:97]
	v_and_b32_e32 v119, 0xffff0000, v103
	v_mul_f32_e32 v93, 0xbfb8aa3b, v96
	v_exp_f32_e32 v98, v93
	v_mul_f32_e32 v93, 0xbfb8aa3b, v97
	v_exp_f32_e32 v99, v93
	v_cvt_pk_bf16_f32 v93, v94, v95
	v_add_f32_e32 v94, 1.0, v98
	v_rcp_f32_e32 v94, v94
	v_add_f32_e32 v95, 1.0, v99
	v_pk_mul_f32 v[98:99], v[50:51], v[132:133]
	v_rcp_f32_e32 v95, v95
	v_pk_fma_f32 v[98:99], v[46:47], v[130:131], v[98:99]
	v_and_b32_dpp v126, v101, v213 row_ror:2 row_mask:0xf bank_mask:0xf bound_ctrl:1
	v_pk_fma_f32 v[98:99], v[38:39], v[118:119], v[98:99]
	v_pk_mul_f32 v[94:95], v[96:97], v[94:95]
	v_pk_add_f32 v[98:99], v[42:43], v[98:99]
	v_pk_mul_f32 v[94:95], v[116:117], v[94:95]
	v_mul_f32_e32 v118, 0xbfb8aa3b, v98
	v_mul_f32_e32 v119, 0xbfb8aa3b, v99
	v_exp_f32_e32 v118, v118
	v_exp_f32_e32 v119, v119
	v_cvt_pk_bf16_f32 v94, v94, v95
	v_and_b32_dpp v117, v100, v221 row_ror:1 row_mask:0xf bank_mask:0xf bound_ctrl:1
	v_add_f32_e32 v118, 1.0, v118
	v_add_f32_e32 v119, 1.0, v119
	v_rcp_f32_e32 v118, v118
	v_rcp_f32_e32 v119, v119
	v_and_b32_dpp v129, v102, v221 row_ror:1 row_mask:0xf bank_mask:0xf bound_ctrl:1
	v_and_b32_dpp v130, v102, v213 row_ror:2 row_mask:0xf bank_mask:0xf bound_ctrl:1
	v_and_b32_dpp v133, v103, v221 row_ror:1 row_mask:0xf bank_mask:0xf bound_ctrl:1
	v_pk_mul_f32 v[96:97], v[98:99], v[118:119]
	v_and_b32_dpp v119, v100, v213 row_ror:2 row_mask:0xf bank_mask:0xf bound_ctrl:1
	v_pk_mul_f32 v[96:97], v[134:135], v[96:97]
	v_and_b32_dpp v134, v103, v213 row_ror:2 row_mask:0xf bank_mask:0xf bound_ctrl:1
	v_cvt_pk_bf16_f32 v95, v96, v97
	global_store_dwordx4 v[162:163], v[92:95], off offset:256
	s_nop 1
	v_mov_b32_e32 v92, v230
	s_waitcnt vmcnt(1)
	v_mov_b32_dpp v99, v104 row_shr:2 row_mask:0xf bank_mask:0xf bound_ctrl:1
	v_mov_b32_dpp v93, v104 row_shr:1 row_mask:0xf bank_mask:0xf bound_ctrl:1
	v_or_b32_sdwa v100, v119, v99 dst_sel:WORD_1 dst_unused:UNUSED_PAD src0_sel:DWORD src1_sel:DWORD
	v_mov_b32_dpp v121, v105 row_shr:1 row_mask:0xf bank_mask:0xf bound_ctrl:1
	v_mov_b32_dpp v123, v105 row_shr:2 row_mask:0xf bank_mask:0xf bound_ctrl:1
	v_mov_b32_dpp v127, v106 row_shr:1 row_mask:0xf bank_mask:0xf bound_ctrl:1
	v_bitop3_b32 v101, v119, s20, v99 bitop3:0xc8
	v_or_b32_sdwa v98, v117, v93 dst_sel:WORD_1 dst_unused:UNUSED_PAD src0_sel:DWORD src1_sel:DWORD
	v_or_b32_sdwa v116, v125, v121 dst_sel:WORD_1 dst_unused:UNUSED_PAD src0_sel:DWORD src1_sel:DWORD
	v_or_b32_sdwa v118, v126, v123 dst_sel:WORD_1 dst_unused:UNUSED_PAD src0_sel:DWORD src1_sel:DWORD
	v_or_b32_sdwa v120, v129, v127 dst_sel:WORD_1 dst_unused:UNUSED_PAD src0_sel:DWORD src1_sel:DWORD
	v_bitop3_b32 v99, v117, s20, v93 bitop3:0xc8
	v_bitop3_b32 v119, v126, s20, v123 bitop3:0xc8
	v_bitop3_b32 v117, v125, s20, v121 bitop3:0xc8
	v_bitop3_b32 v121, v129, s20, v127 bitop3:0xc8
	v_mov_b32_dpp v128, v106 row_shr:2 row_mask:0xf bank_mask:0xf bound_ctrl:1
	v_or_b32_sdwa v102, v130, v128 dst_sel:WORD_1 dst_unused:UNUSED_PAD src0_sel:DWORD src1_sel:DWORD
	v_bitop3_b32 v103, v130, s20, v128 bitop3:0xc8
	v_mov_b32_dpp v132, v107 row_shr:2 row_mask:0xf bank_mask:0xf bound_ctrl:1
	v_mov_b32_dpp v131, v107 row_shr:1 row_mask:0xf bank_mask:0xf bound_ctrl:1
	v_or_b32_sdwa v124, v134, v132 dst_sel:WORD_1 dst_unused:UNUSED_PAD src0_sel:DWORD src1_sel:DWORD
	v_bitop3_b32 v125, v134, s20, v132 bitop3:0xc8
	v_or_b32_sdwa v122, v133, v131 dst_sel:WORD_1 dst_unused:UNUSED_PAD src0_sel:DWORD src1_sel:DWORD
	v_bitop3_b32 v123, v133, s20, v131 bitop3:0xc8
	v_mad_i64_i32 v[94:95], s[18:19], v160, s21, v[204:205]
	v_lshl_add_u64 v[94:95], v[94:95], 0, v[108:109]
	global_load_dwordx4 v[94:97], v[94:95], off
	v_add_u32_e32 v251, 16, v160
	v_mad_i64_i32 v[226:227], s[100:101], v251, s21, v[204:205]
	v_lshl_add_u64 v[226:227], v[226:227], 0, v[108:109]
	global_load_dwordx4 v[226:229], v[226:227], off
	s_waitcnt lgkmcnt(0)
	v_pk_mul_f32 v[126:127], v[86:87], v[92:93] op_sel_hi:[1,0]
	v_pk_mul_f32 v[86:87], v[64:65], v[100:101]
	v_pk_mul_f32 v[90:91], v[90:91], v[92:93] op_sel_hi:[1,0]
	v_pk_fma_f32 v[86:87], v[60:61], v[98:99], v[86:87]
	v_lshlrev_b32_e32 v98, 16, v104
	v_and_b32_e32 v99, 0xffff0000, v104
	v_pk_fma_f32 v[86:87], v[52:53], v[98:99], v[86:87]
	v_pk_mul_f32 v[88:89], v[88:89], v[92:93] op_sel_hi:[1,0]
	v_pk_add_f32 v[86:87], v[56:57], v[86:87]
	v_lshlrev_b32_e32 v100, 16, v105
	v_mul_f32_e32 v93, 0xbfb8aa3b, v86
	v_exp_f32_e32 v98, v93
	v_mul_f32_e32 v93, 0xbfb8aa3b, v87
	v_exp_f32_e32 v99, v93
	v_pk_mul_f32 v[92:93], v[84:85], v[92:93] op_sel_hi:[1,0]
	v_add_f32_e32 v84, 1.0, v98
	v_and_b32_e32 v101, 0xffff0000, v105
	v_add_f32_e32 v85, 1.0, v99
	v_pk_mul_f32 v[98:99], v[66:67], v[118:119]
	v_rcp_f32_e32 v84, v84
	v_pk_fma_f32 v[98:99], v[62:63], v[116:117], v[98:99]
	v_rcp_f32_e32 v85, v85
	v_pk_fma_f32 v[98:99], v[54:55], v[100:101], v[98:99]
	v_and_b32_dpp v117, v105, v164 row_ror:1 row_mask:0xf bank_mask:0xf bound_ctrl:1
	v_pk_add_f32 v[98:99], v[58:59], v[98:99]
	v_pk_mul_f32 v[84:85], v[86:87], v[84:85]
	v_mul_f32_e32 v100, 0xbfb8aa3b, v98
	v_mul_f32_e32 v101, 0xbfb8aa3b, v99
	v_exp_f32_e32 v100, v100
	v_exp_f32_e32 v101, v101
	v_pk_mul_f32 v[84:85], v[84:85], v[88:89]
	v_pk_mul_f32 v[88:89], v[48:49], v[102:103]
	v_add_f32_e32 v100, 1.0, v100
	v_add_f32_e32 v101, 1.0, v101
	v_rcp_f32_e32 v100, v100
	v_rcp_f32_e32 v101, v101
	v_pk_fma_f32 v[88:89], v[44:45], v[120:121], v[88:89]
	v_cvt_pk_bf16_f32 v84, v84, v85
	v_and_b32_dpp v105, v105, v161 row_ror:2 row_mask:0xf bank_mask:0xf bound_ctrl:1
	v_pk_mul_f32 v[86:87], v[98:99], v[100:101]
	v_lshlrev_b32_e32 v98, 16, v107
	v_pk_mul_f32 v[86:87], v[90:91], v[86:87]
	v_lshlrev_b32_e32 v90, 16, v106
	v_and_b32_e32 v91, 0xffff0000, v106
	v_pk_fma_f32 v[88:89], v[36:37], v[90:91], v[88:89]
	v_and_b32_e32 v99, 0xffff0000, v107
	v_pk_add_f32 v[88:89], v[40:41], v[88:89]
	v_and_b32_dpp v120, v106, v164 row_ror:1 row_mask:0xf bank_mask:0xf bound_ctrl:1
	v_mul_f32_e32 v85, 0xbfb8aa3b, v88
	v_exp_f32_e32 v90, v85
	v_mul_f32_e32 v85, 0xbfb8aa3b, v89
	v_exp_f32_e32 v91, v85
	v_cvt_pk_bf16_f32 v85, v86, v87
	v_add_f32_e32 v86, 1.0, v90
	v_rcp_f32_e32 v86, v86
	v_add_f32_e32 v87, 1.0, v91
	v_pk_mul_f32 v[90:91], v[50:51], v[124:125]
	v_rcp_f32_e32 v87, v87
	v_pk_fma_f32 v[90:91], v[46:47], v[122:123], v[90:91]
	v_and_b32_dpp v121, v106, v161 row_ror:2 row_mask:0xf bank_mask:0xf bound_ctrl:1
	v_pk_fma_f32 v[90:91], v[38:39], v[98:99], v[90:91]
	v_pk_mul_f32 v[86:87], v[88:89], v[86:87]
	v_pk_add_f32 v[90:91], v[42:43], v[90:91]
	v_pk_mul_f32 v[86:87], v[92:93], v[86:87]
	v_mul_f32_e32 v98, 0xbfb8aa3b, v90
	v_mul_f32_e32 v99, 0xbfb8aa3b, v91
	v_exp_f32_e32 v98, v98
	v_exp_f32_e32 v99, v99
	v_cvt_pk_bf16_f32 v86, v86, v87
	v_and_b32_dpp v93, v104, v161 row_ror:2 row_mask:0xf bank_mask:0xf bound_ctrl:1
	v_add_f32_e32 v98, 1.0, v98
	v_add_f32_e32 v99, 1.0, v99
	v_rcp_f32_e32 v98, v98
	v_rcp_f32_e32 v99, v99
	v_and_b32_dpp v124, v107, v164 row_ror:1 row_mask:0xf bank_mask:0xf bound_ctrl:1
	v_and_b32_dpp v107, v107, v161 row_ror:2 row_mask:0xf bank_mask:0xf bound_ctrl:1
	v_pk_mul_f32 v[88:89], v[90:91], v[98:99]
	s_nop 0
	v_pk_mul_f32 v[88:89], v[126:127], v[88:89]
	v_and_b32_dpp v99, v104, v164 row_ror:1 row_mask:0xf bank_mask:0xf bound_ctrl:1
	v_cvt_pk_bf16_f32 v87, v88, v89
	global_store_dwordx4 v[148:149], v[84:87], off offset:256
	v_mov_b32_e32 v88, v231
	s_nop 0
	v_mad_i64_i32 v[84:85], s[18:19], v152, s21, v[204:205]
	v_lshl_add_u64 v[84:85], v[84:85], 0, v[108:109]
	s_waitcnt vmcnt(1)
	v_mov_b32_e32 v84, v226
	v_mov_b32_e32 v85, v227
	v_mov_b32_e32 v86, v228
	v_mov_b32_e32 v87, v229
	s_nop 1
	v_mov_b32_dpp v91, v94 row_shr:2 row_mask:0xf bank_mask:0xf bound_ctrl:1
	v_mov_b32_dpp v89, v94 row_shr:1 row_mask:0xf bank_mask:0xf bound_ctrl:1
	v_or_b32_sdwa v92, v93, v91 dst_sel:WORD_1 dst_unused:UNUSED_PAD src0_sel:DWORD src1_sel:DWORD
	v_mov_b32_dpp v103, v95 row_shr:1 row_mask:0xf bank_mask:0xf bound_ctrl:1
	v_mov_b32_dpp v101, v95 row_shr:2 row_mask:0xf bank_mask:0xf bound_ctrl:1
	v_mov_b32_dpp v118, v96 row_shr:1 row_mask:0xf bank_mask:0xf bound_ctrl:1
	v_mov_b32_dpp v119, v96 row_shr:2 row_mask:0xf bank_mask:0xf bound_ctrl:1
	v_bitop3_b32 v93, v93, s20, v91 bitop3:0xc8
	v_or_b32_sdwa v90, v99, v89 dst_sel:WORD_1 dst_unused:UNUSED_PAD src0_sel:DWORD src1_sel:DWORD
	v_or_b32_sdwa v98, v117, v103 dst_sel:WORD_1 dst_unused:UNUSED_PAD src0_sel:DWORD src1_sel:DWORD
	v_or_b32_sdwa v100, v105, v101 dst_sel:WORD_1 dst_unused:UNUSED_PAD src0_sel:DWORD src1_sel:DWORD
	v_or_b32_sdwa v102, v120, v118 dst_sel:WORD_1 dst_unused:UNUSED_PAD src0_sel:DWORD src1_sel:DWORD
	v_or_b32_sdwa v104, v121, v119 dst_sel:WORD_1 dst_unused:UNUSED_PAD src0_sel:DWORD src1_sel:DWORD
	v_bitop3_b32 v91, v99, s20, v89 bitop3:0xc8
	v_bitop3_b32 v101, v105, s20, v101 bitop3:0xc8
	v_bitop3_b32 v99, v117, s20, v103 bitop3:0xc8
	v_bitop3_b32 v105, v121, s20, v119 bitop3:0xc8
	v_bitop3_b32 v103, v120, s20, v118 bitop3:0xc8
	v_mov_b32_dpp v123, v97 row_shr:2 row_mask:0xf bank_mask:0xf bound_ctrl:1
	v_mov_b32_dpp v122, v97 row_shr:1 row_mask:0xf bank_mask:0xf bound_ctrl:1
	v_or_b32_sdwa v116, v107, v123 dst_sel:WORD_1 dst_unused:UNUSED_PAD src0_sel:DWORD src1_sel:DWORD
	v_bitop3_b32 v117, v107, s20, v123 bitop3:0xc8
	v_or_b32_sdwa v106, v124, v122 dst_sel:WORD_1 dst_unused:UNUSED_PAD src0_sel:DWORD src1_sel:DWORD
	v_bitop3_b32 v107, v124, s20, v122 bitop3:0xc8
	s_waitcnt lgkmcnt(0)
	v_pk_mul_f32 v[118:119], v[78:79], v[88:89] op_sel_hi:[1,0]
	v_pk_mul_f32 v[78:79], v[64:65], v[92:93]
	v_pk_mul_f32 v[82:83], v[82:83], v[88:89] op_sel_hi:[1,0]
	v_pk_fma_f32 v[78:79], v[60:61], v[90:91], v[78:79]
	v_lshlrev_b32_e32 v90, 16, v94
	v_and_b32_e32 v91, 0xffff0000, v94
	v_pk_fma_f32 v[78:79], v[52:53], v[90:91], v[78:79]
	v_pk_mul_f32 v[80:81], v[80:81], v[88:89] op_sel_hi:[1,0]
	v_pk_add_f32 v[78:79], v[56:57], v[78:79]
	v_lshlrev_b32_e32 v92, 16, v95
	v_mul_f32_e32 v89, 0xbfb8aa3b, v78
	v_exp_f32_e32 v90, v89
	v_mul_f32_e32 v89, 0xbfb8aa3b, v79
	v_exp_f32_e32 v91, v89
	v_pk_mul_f32 v[88:89], v[76:77], v[88:89] op_sel_hi:[1,0]
	v_add_f32_e32 v76, 1.0, v90
	v_and_b32_e32 v93, 0xffff0000, v95
	v_add_f32_e32 v77, 1.0, v91
	v_pk_mul_f32 v[90:91], v[66:67], v[100:101]
	v_rcp_f32_e32 v76, v76
	v_pk_fma_f32 v[90:91], v[62:63], v[98:99], v[90:91]
	v_rcp_f32_e32 v77, v77
	v_pk_fma_f32 v[90:91], v[54:55], v[92:93], v[90:91]
	v_mov_b32_dpp v98, v86 row_shr:1 row_mask:0xf bank_mask:0xf bound_ctrl:1
	v_pk_add_f32 v[90:91], v[58:59], v[90:91]
	v_pk_mul_f32 v[76:77], v[78:79], v[76:77]
	v_mul_f32_e32 v92, 0xbfb8aa3b, v90
	v_mul_f32_e32 v93, 0xbfb8aa3b, v91
	v_exp_f32_e32 v92, v92
	v_exp_f32_e32 v93, v93
	v_pk_mul_f32 v[76:77], v[76:77], v[80:81]
	v_pk_mul_f32 v[80:81], v[48:49], v[104:105]
	v_add_f32_e32 v92, 1.0, v92
	v_add_f32_e32 v93, 1.0, v93
	v_rcp_f32_e32 v92, v92
	v_rcp_f32_e32 v93, v93
	v_pk_fma_f32 v[80:81], v[44:45], v[102:103], v[80:81]
	v_cvt_pk_bf16_f32 v76, v76, v77
	v_mov_b32_dpp v99, v86 row_shr:2 row_mask:0xf bank_mask:0xf bound_ctrl:1
	v_pk_mul_f32 v[78:79], v[90:91], v[92:93]
	v_lshlrev_b32_e32 v90, 16, v97
	v_pk_mul_f32 v[78:79], v[82:83], v[78:79]
	v_lshlrev_b32_e32 v82, 16, v96
	v_and_b32_e32 v83, 0xffff0000, v96
	v_pk_fma_f32 v[80:81], v[36:37], v[82:83], v[80:81]
	v_and_b32_e32 v91, 0xffff0000, v97
	v_pk_add_f32 v[80:81], v[40:41], v[80:81]
	v_mov_b32_dpp v92, v96 row_ror:2 row_mask:0xf bank_mask:0xf bound_ctrl:1
	v_mul_f32_e32 v77, 0xbfb8aa3b, v80
	v_exp_f32_e32 v82, v77
	v_mul_f32_e32 v77, 0xbfb8aa3b, v81
	v_exp_f32_e32 v83, v77
	v_cvt_pk_bf16_f32 v77, v78, v79
	v_add_f32_e32 v78, 1.0, v82
	v_rcp_f32_e32 v78, v78
	v_add_f32_e32 v79, 1.0, v83
	v_pk_mul_f32 v[82:83], v[50:51], v[116:117]
	v_rcp_f32_e32 v79, v79
	v_pk_fma_f32 v[82:83], v[46:47], v[106:107], v[82:83]
	v_cndmask_b32_e64 v101, 0, v92, s[38:39]
	v_pk_fma_f32 v[82:83], v[38:39], v[90:91], v[82:83]
	v_pk_mul_f32 v[78:79], v[80:81], v[78:79]
	v_pk_add_f32 v[82:83], v[42:43], v[82:83]
	v_pk_mul_f32 v[78:79], v[88:89], v[78:79]
	v_mul_f32_e32 v90, 0xbfb8aa3b, v82
	v_mul_f32_e32 v91, 0xbfb8aa3b, v83
	v_exp_f32_e32 v90, v90
	v_exp_f32_e32 v91, v91
	v_cvt_pk_bf16_f32 v78, v78, v79
	v_or_b32_sdwa v92, v101, v99 dst_sel:WORD_1 dst_unused:UNUSED_PAD src0_sel:DWORD src1_sel:DWORD
	v_add_f32_e32 v90, 1.0, v90
	v_add_f32_e32 v91, 1.0, v91
	v_rcp_f32_e32 v90, v90
	v_rcp_f32_e32 v91, v91
	v_mov_b32_dpp v88, v95 row_ror:2 row_mask:0xf bank_mask:0xf bound_ctrl:1
	v_mov_b32_dpp v89, v85 row_shr:2 row_mask:0xf bank_mask:0xf bound_ctrl:1
	v_mov_b32_dpp v103, v87 row_shr:2 row_mask:0xf bank_mask:0xf bound_ctrl:1
	v_pk_mul_f32 v[80:81], v[82:83], v[90:91]
	v_mov_b32_dpp v82, v95 row_ror:1 row_mask:0xf bank_mask:0xf bound_ctrl:1
	v_pk_mul_f32 v[80:81], v[118:119], v[80:81]
	v_mov_b32_dpp v90, v96 row_ror:1 row_mask:0xf bank_mask:0xf bound_ctrl:1
	v_cvt_pk_bf16_f32 v79, v80, v81
	global_store_dwordx4 v[142:143], v[76:79], off offset:256
	s_nop 1
	v_mov_b32_e32 v76, v240
	v_mov_b32_dpp v80, v94 row_ror:2 row_mask:0xf bank_mask:0xf bound_ctrl:1
	v_mov_b32_dpp v78, v94 row_ror:1 row_mask:0xf bank_mask:0xf bound_ctrl:1
	v_mov_b32_dpp v79, v84 row_shr:2 row_mask:0xf bank_mask:0xf bound_ctrl:1
	v_cndmask_b32_e64 v81, 0, v80, s[38:39]
	v_mov_b32_dpp v77, v84 row_shr:1 row_mask:0xf bank_mask:0xf bound_ctrl:1
	v_cndmask_b32_e64 v83, 0, v78, s[36:37]
	v_or_b32_sdwa v80, v81, v79 dst_sel:WORD_1 dst_unused:UNUSED_PAD src0_sel:DWORD src1_sel:DWORD
	v_mov_b32_dpp v91, v85 row_shr:1 row_mask:0xf bank_mask:0xf bound_ctrl:1
	v_cndmask_b32_e64 v93, 0, v82, s[36:37]
	v_cndmask_b32_e64 v100, 0, v90, s[36:37]
	v_bitop3_b32 v81, v81, s20, v79 bitop3:0xc8
	v_or_b32_sdwa v78, v83, v77 dst_sel:WORD_1 dst_unused:UNUSED_PAD src0_sel:DWORD src1_sel:DWORD
	v_or_b32_sdwa v82, v93, v91 dst_sel:WORD_1 dst_unused:UNUSED_PAD src0_sel:DWORD src1_sel:DWORD
	v_or_b32_sdwa v90, v100, v98 dst_sel:WORD_1 dst_unused:UNUSED_PAD src0_sel:DWORD src1_sel:DWORD
	v_bitop3_b32 v79, v83, s20, v77 bitop3:0xc8
	v_bitop3_b32 v83, v93, s20, v91 bitop3:0xc8
	v_bitop3_b32 v93, v101, s20, v99 bitop3:0xc8
	v_bitop3_b32 v91, v100, s20, v98 bitop3:0xc8
	v_cndmask_b32_e64 v95, 0, v88, s[38:39]
	v_or_b32_sdwa v88, v95, v89 dst_sel:WORD_1 dst_unused:UNUSED_PAD src0_sel:DWORD src1_sel:DWORD
	v_bitop3_b32 v89, v95, s20, v89 bitop3:0xc8
	v_mov_b32_dpp v96, v97 row_ror:2 row_mask:0xf bank_mask:0xf bound_ctrl:1
	v_mov_b32_dpp v94, v97 row_ror:1 row_mask:0xf bank_mask:0xf bound_ctrl:1
	v_cndmask_b32_e64 v97, 0, v96, s[38:39]
	v_mov_b32_dpp v102, v87 row_shr:1 row_mask:0xf bank_mask:0xf bound_ctrl:1
	v_cndmask_b32_e64 v104, 0, v94, s[36:37]
	v_or_b32_sdwa v96, v97, v103 dst_sel:WORD_1 dst_unused:UNUSED_PAD src0_sel:DWORD src1_sel:DWORD
	v_bitop3_b32 v97, v97, s20, v103 bitop3:0xc8
	v_or_b32_sdwa v94, v104, v102 dst_sel:WORD_1 dst_unused:UNUSED_PAD src0_sel:DWORD src1_sel:DWORD
	v_bitop3_b32 v95, v104, s20, v102 bitop3:0xc8
	s_waitcnt lgkmcnt(0)
	v_pk_mul_f32 v[98:99], v[70:71], v[76:77] op_sel_hi:[1,0]
	v_pk_mul_f32 v[70:71], v[64:65], v[80:81]
	v_pk_mul_f32 v[74:75], v[74:75], v[76:77] op_sel_hi:[1,0]
	v_pk_fma_f32 v[70:71], v[60:61], v[78:79], v[70:71]
	v_lshlrev_b32_e32 v78, 16, v84
	v_and_b32_e32 v79, 0xffff0000, v84
	v_pk_fma_f32 v[70:71], v[52:53], v[78:79], v[70:71]
	v_pk_mul_f32 v[72:73], v[72:73], v[76:77] op_sel_hi:[1,0]
	v_pk_add_f32 v[70:71], v[56:57], v[70:71]
	v_lshlrev_b32_e32 v80, 16, v85
	v_mul_f32_e32 v77, 0xbfb8aa3b, v70
	v_exp_f32_e32 v78, v77
	v_mul_f32_e32 v77, 0xbfb8aa3b, v71
	v_exp_f32_e32 v79, v77
	v_pk_mul_f32 v[76:77], v[68:69], v[76:77] op_sel_hi:[1,0]
	v_add_f32_e32 v68, 1.0, v78
	v_and_b32_e32 v81, 0xffff0000, v85
	v_add_f32_e32 v69, 1.0, v79
	v_pk_mul_f32 v[78:79], v[66:67], v[88:89]
	v_rcp_f32_e32 v68, v68
	v_pk_fma_f32 v[78:79], v[62:63], v[82:83], v[78:79]
	v_rcp_f32_e32 v69, v69
	v_pk_fma_f32 v[78:79], v[54:55], v[80:81], v[78:79]
	v_pk_mul_f32 v[68:69], v[70:71], v[68:69]
	v_pk_add_f32 v[78:79], v[58:59], v[78:79]
	v_pk_mul_f32 v[68:69], v[68:69], v[72:73]
	v_mul_f32_e32 v80, 0xbfb8aa3b, v78
	v_mul_f32_e32 v81, 0xbfb8aa3b, v79
	v_exp_f32_e32 v80, v80
	v_exp_f32_e32 v81, v81
	v_pk_mul_f32 v[72:73], v[48:49], v[92:93]
	v_cvt_pk_bf16_f32 v68, v68, v69
	v_add_f32_e32 v80, 1.0, v80
	v_add_f32_e32 v81, 1.0, v81
	v_rcp_f32_e32 v80, v80
	v_rcp_f32_e32 v81, v81
	v_pk_fma_f32 v[72:73], v[44:45], v[90:91], v[72:73]
	v_pk_mul_f32 v[70:71], v[78:79], v[80:81]
	s_nop 0
	v_pk_mul_f32 v[70:71], v[74:75], v[70:71]
	v_lshlrev_b32_e32 v74, 16, v86
	v_and_b32_e32 v75, 0xffff0000, v86
	v_pk_fma_f32 v[72:73], v[36:37], v[74:75], v[72:73]
	v_lshlrev_b32_e32 v78, 16, v87
	v_pk_add_f32 v[72:73], v[40:41], v[72:73]
	v_and_b32_e32 v79, 0xffff0000, v87
	v_mul_f32_e32 v69, 0xbfb8aa3b, v72
	v_exp_f32_e32 v74, v69
	v_mul_f32_e32 v69, 0xbfb8aa3b, v73
	v_exp_f32_e32 v75, v69
	v_cvt_pk_bf16_f32 v69, v70, v71
	v_add_f32_e32 v70, 1.0, v74
	v_rcp_f32_e32 v70, v70
	v_add_f32_e32 v71, 1.0, v75
	v_pk_mul_f32 v[74:75], v[50:51], v[96:97]
	v_rcp_f32_e32 v71, v71
	v_pk_fma_f32 v[74:75], v[46:47], v[94:95], v[74:75]
	v_pk_mul_f32 v[70:71], v[72:73], v[70:71]
	v_pk_fma_f32 v[74:75], v[38:39], v[78:79], v[74:75]
	v_pk_mul_f32 v[70:71], v[76:77], v[70:71]
	v_pk_add_f32 v[74:75], v[42:43], v[74:75]
	v_cvt_pk_bf16_f32 v70, v70, v71
	v_mul_f32_e32 v78, 0xbfb8aa3b, v74
	v_mul_f32_e32 v79, 0xbfb8aa3b, v75
	v_exp_f32_e32 v78, v78
	v_exp_f32_e32 v79, v79
	v_mad_i64_i32 v[76:77], s[18:19], v159, s21, v[204:205]
	v_add_f32_e32 v78, 1.0, v78
	v_add_f32_e32 v79, 1.0, v79
	v_rcp_f32_e32 v78, v78
	v_rcp_f32_e32 v79, v79
	v_lshl_add_u64 v[76:77], v[76:77], 0, v[108:109]
	v_pk_mul_f32 v[72:73], v[74:75], v[78:79]
	s_nop 0
	v_pk_mul_f32 v[72:73], v[98:99], v[72:73]
	s_nop 0
	v_cvt_pk_bf16_f32 v71, v72, v73
	v_mad_i64_i32 v[72:73], s[18:19], v165, s21, v[204:205]
	v_lshl_add_u64 v[72:73], v[72:73], 0, v[108:109]
	global_load_dwordx4 v[72:75], v[72:73], off
	s_nop 0
	global_store_dwordx4 v[136:137], v[68:71], off offset:256
	global_load_dwordx4 v[68:71], v[140:141], off offset:256
	s_nop 0
	global_load_dword v80, v[202:203], off offset:512
	global_load_dword v230, v[202:203], off offset:576
	global_load_dword v231, v[202:203], off offset:640
	global_load_dword v240, v[202:203], off offset:704
	s_waitcnt lgkmcnt(0)
	s_waitcnt vmcnt(6)
	v_mov_b32_dpp v83, v72 row_shr:2 row_mask:0xf bank_mask:0xf bound_ctrl:1
	v_mov_b32_dpp v81, v72 row_shr:1 row_mask:0xf bank_mask:0xf bound_ctrl:1
	s_waitcnt vmcnt(4)
	v_and_b32_dpp v87, v68, v157 row_ror:2 row_mask:0xf bank_mask:0xf bound_ctrl:1
	v_and_b32_dpp v85, v68, v158 row_ror:1 row_mask:0xf bank_mask:0xf bound_ctrl:1
	v_or_b32_sdwa v68, v87, v83 dst_sel:WORD_1 dst_unused:UNUSED_PAD src0_sel:DWORD src1_sel:DWORD
	v_mov_b32_dpp v89, v73 row_shr:1 row_mask:0xf bank_mask:0xf bound_ctrl:1
	v_mov_b32_dpp v91, v73 row_shr:2 row_mask:0xf bank_mask:0xf bound_ctrl:1
	v_and_b32_dpp v93, v69, v158 row_ror:1 row_mask:0xf bank_mask:0xf bound_ctrl:1
	v_and_b32_dpp v94, v69, v157 row_ror:2 row_mask:0xf bank_mask:0xf bound_ctrl:1
	v_mov_b32_dpp v95, v74 row_shr:1 row_mask:0xf bank_mask:0xf bound_ctrl:1
	v_and_b32_dpp v97, v70, v158 row_ror:1 row_mask:0xf bank_mask:0xf bound_ctrl:1
	v_bitop3_b32 v69, v87, s20, v83 bitop3:0xc8
	v_or_b32_sdwa v82, v85, v81 dst_sel:WORD_1 dst_unused:UNUSED_PAD src0_sel:DWORD src1_sel:DWORD
	v_or_b32_sdwa v84, v93, v89 dst_sel:WORD_1 dst_unused:UNUSED_PAD src0_sel:DWORD src1_sel:DWORD
	v_or_b32_sdwa v86, v94, v91 dst_sel:WORD_1 dst_unused:UNUSED_PAD src0_sel:DWORD src1_sel:DWORD
	v_or_b32_sdwa v88, v97, v95 dst_sel:WORD_1 dst_unused:UNUSED_PAD src0_sel:DWORD src1_sel:DWORD
	v_bitop3_b32 v83, v85, s20, v81 bitop3:0xc8
	v_bitop3_b32 v87, v94, s20, v91 bitop3:0xc8
	v_bitop3_b32 v85, v93, s20, v89 bitop3:0xc8
	v_bitop3_b32 v89, v97, s20, v95 bitop3:0xc8
	s_waitcnt vmcnt(3)
	v_pk_mul_f32 v[94:95], v[30:31], v[80:81] op_sel_hi:[1,0]
	v_pk_mul_f32 v[30:31], v[64:65], v[68:69]
	v_lshlrev_b32_e32 v68, 16, v72
	v_pk_fma_f32 v[30:31], v[60:61], v[82:83], v[30:31]
	v_and_b32_e32 v69, 0xffff0000, v72
	v_pk_fma_f32 v[30:31], v[52:53], v[68:69], v[30:31]
	v_pk_mul_f32 v[34:35], v[34:35], v[80:81] op_sel_hi:[1,0]
	v_pk_add_f32 v[30:31], v[56:57], v[30:31]
	v_pk_mul_f32 v[32:33], v[32:33], v[80:81] op_sel_hi:[1,0]
	v_mul_f32_e32 v68, 0xbfb8aa3b, v30
	v_exp_f32_e32 v81, v68
	v_mul_f32_e32 v68, 0xbfb8aa3b, v31
	v_exp_f32_e32 v82, v68
	v_and_b32_e32 v83, 0xffff0000, v73
	v_pk_mul_f32 v[68:69], v[28:29], v[80:81] op_sel_hi:[1,0]
	v_add_f32_e32 v28, 1.0, v81
	v_pk_mul_f32 v[80:81], v[66:67], v[86:87]
	v_add_f32_e32 v29, 1.0, v82
	v_pk_fma_f32 v[80:81], v[62:63], v[84:85], v[80:81]
	v_lshlrev_b32_e32 v82, 16, v73
	v_pk_fma_f32 v[80:81], v[54:55], v[82:83], v[80:81]
	v_rcp_f32_e32 v28, v28
	v_pk_add_f32 v[80:81], v[58:59], v[80:81]
	v_rcp_f32_e32 v29, v29
	v_mul_f32_e32 v82, 0xbfb8aa3b, v80
	v_mul_f32_e32 v83, 0xbfb8aa3b, v81
	v_exp_f32_e32 v82, v82
	v_exp_f32_e32 v83, v83
	v_mov_b32_dpp v96, v74 row_shr:2 row_mask:0xf bank_mask:0xf bound_ctrl:1
	v_and_b32_dpp v98, v70, v157 row_ror:2 row_mask:0xf bank_mask:0xf bound_ctrl:1
	v_add_f32_e32 v82, 1.0, v82
	v_add_f32_e32 v83, 1.0, v83
	v_rcp_f32_e32 v82, v82
	v_rcp_f32_e32 v83, v83
	v_or_b32_sdwa v70, v98, v96 dst_sel:WORD_1 dst_unused:UNUSED_PAD src0_sel:DWORD src1_sel:DWORD
	v_and_b32_dpp v101, v71, v158 row_ror:1 row_mask:0xf bank_mask:0xf bound_ctrl:1
	v_and_b32_dpp v102, v71, v157 row_ror:2 row_mask:0xf bank_mask:0xf bound_ctrl:1
	v_bitop3_b32 v71, v98, s20, v96 bitop3:0xc8
	v_pk_mul_f32 v[28:29], v[30:31], v[28:29]
	v_pk_mul_f32 v[30:31], v[80:81], v[82:83]
	v_pk_mul_f32 v[28:29], v[28:29], v[32:33]
	v_pk_mul_f32 v[32:33], v[48:49], v[70:71]
	v_pk_mul_f32 v[30:31], v[34:35], v[30:31]
	v_pk_fma_f32 v[32:33], v[44:45], v[88:89], v[32:33]
	v_lshlrev_b32_e32 v34, 16, v74
	v_and_b32_e32 v35, 0xffff0000, v74
	v_pk_fma_f32 v[32:33], v[36:37], v[34:35], v[32:33]
	v_cvt_pk_bf16_f32 v28, v28, v29
	v_pk_add_f32 v[32:33], v[40:41], v[32:33]
	v_mov_b32_dpp v100, v75 row_shr:2 row_mask:0xf bank_mask:0xf bound_ctrl:1
	v_mul_f32_e32 v29, 0xbfb8aa3b, v32
	v_exp_f32_e32 v34, v29
	v_mul_f32_e32 v29, 0xbfb8aa3b, v33
	v_exp_f32_e32 v35, v29
	v_mov_b32_dpp v99, v75 row_shr:1 row_mask:0xf bank_mask:0xf bound_ctrl:1
	v_or_b32_sdwa v92, v102, v100 dst_sel:WORD_1 dst_unused:UNUSED_PAD src0_sel:DWORD src1_sel:DWORD
	v_bitop3_b32 v93, v102, s20, v100 bitop3:0xc8
	v_or_b32_sdwa v90, v101, v99 dst_sel:WORD_1 dst_unused:UNUSED_PAD src0_sel:DWORD src1_sel:DWORD
	v_bitop3_b32 v91, v101, s20, v99 bitop3:0xc8
	v_cvt_pk_bf16_f32 v29, v30, v31
	v_add_f32_e32 v30, 1.0, v34
	v_add_f32_e32 v31, 1.0, v35
	v_pk_mul_f32 v[34:35], v[50:51], v[92:93]
	v_lshlrev_b32_e32 v70, 16, v75
	v_pk_fma_f32 v[34:35], v[46:47], v[90:91], v[34:35]
	v_and_b32_e32 v71, 0xffff0000, v75
	v_pk_fma_f32 v[34:35], v[38:39], v[70:71], v[34:35]
	v_rcp_f32_e32 v30, v30
	v_pk_add_f32 v[34:35], v[42:43], v[34:35]
	v_rcp_f32_e32 v31, v31
	v_mul_f32_e32 v70, 0xbfb8aa3b, v34
	v_mul_f32_e32 v71, 0xbfb8aa3b, v35
	v_exp_f32_e32 v70, v70
	v_exp_f32_e32 v71, v71
	v_pk_mul_f32 v[30:31], v[32:33], v[30:31]
	global_load_dwordx4 v[76:79], v[76:77], off
	v_add_f32_e32 v70, 1.0, v70
	v_add_f32_e32 v71, 1.0, v71
	v_rcp_f32_e32 v70, v70
	v_rcp_f32_e32 v71, v71
	v_pk_mul_f32 v[30:31], v[68:69], v[30:31]
	v_and_b32_dpp v69, v72, v154 row_ror:2 row_mask:0xf bank_mask:0xf bound_ctrl:1
	v_cvt_pk_bf16_f32 v30, v30, v31
	v_pk_mul_f32 v[32:33], v[34:35], v[70:71]
	v_and_b32_dpp v71, v72, v155 row_ror:1 row_mask:0xf bank_mask:0xf bound_ctrl:1
	v_pk_mul_f32 v[32:33], v[94:95], v[32:33]
	v_and_b32_dpp v85, v73, v155 row_ror:1 row_mask:0xf bank_mask:0xf bound_ctrl:1
	v_cvt_pk_bf16_f32 v31, v32, v33
	global_store_dwordx4 v[138:139], v[28:31], off offset:256
	s_waitcnt vmcnt(4)
	v_mov_b32_e32 v32, v230
	v_and_b32_dpp v88, v74, v155 row_ror:1 row_mask:0xf bank_mask:0xf bound_ctrl:1
	v_and_b32_dpp v89, v74, v154 row_ror:2 row_mask:0xf bank_mask:0xf bound_ctrl:1
	v_and_b32_dpp v92, v75, v155 row_ror:1 row_mask:0xf bank_mask:0xf bound_ctrl:1
	v_and_b32_dpp v93, v75, v154 row_ror:2 row_mask:0xf bank_mask:0xf bound_ctrl:1
	v_and_b32_dpp v73, v73, v154 row_ror:2 row_mask:0xf bank_mask:0xf bound_ctrl:1
	v_mad_i64_i32 v[28:29], s[18:19], v156, s21, v[204:205]
	v_lshl_add_u64 v[28:29], v[28:29], 0, v[108:109]
	global_load_dwordx4 v[28:31], v[28:29], off
	v_add_u32_e32 v251, 16, v156
	v_mad_i64_i32 v[226:227], s[100:101], v251, s21, v[204:205]
	v_lshl_add_u64 v[226:227], v[226:227], 0, v[108:109]
	global_load_dwordx4 v[226:229], v[226:227], off
	s_waitcnt lgkmcnt(0)
	s_waitcnt vmcnt(3)
	v_mov_b32_dpp v35, v76 row_shr:2 row_mask:0xf bank_mask:0xf bound_ctrl:1
	v_mov_b32_dpp v33, v76 row_shr:1 row_mask:0xf bank_mask:0xf bound_ctrl:1
	v_or_b32_sdwa v68, v69, v35 dst_sel:WORD_1 dst_unused:UNUSED_PAD src0_sel:DWORD src1_sel:DWORD
	v_mov_b32_dpp v81, v77 row_shr:1 row_mask:0xf bank_mask:0xf bound_ctrl:1
	v_mov_b32_dpp v86, v78 row_shr:1 row_mask:0xf bank_mask:0xf bound_ctrl:1
	v_mov_b32_dpp v87, v78 row_shr:2 row_mask:0xf bank_mask:0xf bound_ctrl:1
	v_bitop3_b32 v69, v69, s20, v35 bitop3:0xc8
	v_or_b32_sdwa v34, v71, v33 dst_sel:WORD_1 dst_unused:UNUSED_PAD src0_sel:DWORD src1_sel:DWORD
	v_or_b32_sdwa v70, v85, v81 dst_sel:WORD_1 dst_unused:UNUSED_PAD src0_sel:DWORD src1_sel:DWORD
	v_or_b32_sdwa v80, v88, v86 dst_sel:WORD_1 dst_unused:UNUSED_PAD src0_sel:DWORD src1_sel:DWORD
	v_or_b32_sdwa v74, v89, v87 dst_sel:WORD_1 dst_unused:UNUSED_PAD src0_sel:DWORD src1_sel:DWORD
	v_bitop3_b32 v35, v71, s20, v33 bitop3:0xc8
	v_bitop3_b32 v71, v85, s20, v81 bitop3:0xc8
	v_bitop3_b32 v75, v89, s20, v87 bitop3:0xc8
	v_bitop3_b32 v81, v88, s20, v86 bitop3:0xc8
	v_pk_mul_f32 v[86:87], v[22:23], v[32:33] op_sel_hi:[1,0]
	v_pk_mul_f32 v[22:23], v[64:65], v[68:69]
	v_pk_mul_f32 v[26:27], v[26:27], v[32:33] op_sel_hi:[1,0]
	v_pk_fma_f32 v[22:23], v[60:61], v[34:35], v[22:23]
	v_lshlrev_b32_e32 v34, 16, v76
	v_and_b32_e32 v35, 0xffff0000, v76
	v_pk_fma_f32 v[22:23], v[52:53], v[34:35], v[22:23]
	v_pk_mul_f32 v[24:25], v[24:25], v[32:33] op_sel_hi:[1,0]
	v_pk_add_f32 v[22:23], v[56:57], v[22:23]
	v_mov_b32_dpp v83, v77 row_shr:2 row_mask:0xf bank_mask:0xf bound_ctrl:1
	v_mul_f32_e32 v33, 0xbfb8aa3b, v22
	v_exp_f32_e32 v34, v33
	v_mul_f32_e32 v33, 0xbfb8aa3b, v23
	v_exp_f32_e32 v35, v33
	v_or_b32_sdwa v72, v73, v83 dst_sel:WORD_1 dst_unused:UNUSED_PAD src0_sel:DWORD src1_sel:DWORD
	v_bitop3_b32 v73, v73, s20, v83 bitop3:0xc8
	v_pk_mul_f32 v[32:33], v[20:21], v[32:33] op_sel_hi:[1,0]
	v_add_f32_e32 v20, 1.0, v34
	v_add_f32_e32 v21, 1.0, v35
	v_pk_mul_f32 v[34:35], v[66:67], v[72:73]
	v_lshlrev_b32_e32 v68, 16, v77
	v_pk_fma_f32 v[34:35], v[62:63], v[70:71], v[34:35]
	v_and_b32_e32 v69, 0xffff0000, v77
	v_pk_fma_f32 v[34:35], v[54:55], v[68:69], v[34:35]
	v_rcp_f32_e32 v20, v20
	v_pk_add_f32 v[34:35], v[58:59], v[34:35]
	v_rcp_f32_e32 v21, v21
	v_mul_f32_e32 v68, 0xbfb8aa3b, v34
	v_mul_f32_e32 v69, 0xbfb8aa3b, v35
	v_exp_f32_e32 v68, v68
	v_exp_f32_e32 v69, v69
	v_pk_mul_f32 v[20:21], v[22:23], v[20:21]
	v_mov_b32_dpp v91, v79 row_shr:2 row_mask:0xf bank_mask:0xf bound_ctrl:1
	v_add_f32_e32 v68, 1.0, v68
	v_add_f32_e32 v69, 1.0, v69
	v_rcp_f32_e32 v68, v68
	v_rcp_f32_e32 v69, v69
	v_pk_mul_f32 v[20:21], v[20:21], v[24:25]
	v_pk_mul_f32 v[24:25], v[48:49], v[74:75]
	v_cvt_pk_bf16_f32 v20, v20, v21
	v_pk_mul_f32 v[22:23], v[34:35], v[68:69]
	v_pk_fma_f32 v[24:25], v[44:45], v[80:81], v[24:25]
	v_pk_mul_f32 v[22:23], v[26:27], v[22:23]
	v_lshlrev_b32_e32 v26, 16, v78
	v_and_b32_e32 v27, 0xffff0000, v78
	v_pk_fma_f32 v[24:25], v[36:37], v[26:27], v[24:25]
	v_mov_b32_dpp v90, v79 row_shr:1 row_mask:0xf bank_mask:0xf bound_ctrl:1
	v_pk_add_f32 v[24:25], v[40:41], v[24:25]
	v_or_b32_sdwa v84, v93, v91 dst_sel:WORD_1 dst_unused:UNUSED_PAD src0_sel:DWORD src1_sel:DWORD
	v_mul_f32_e32 v21, 0xbfb8aa3b, v24
	v_exp_f32_e32 v26, v21
	v_mul_f32_e32 v21, 0xbfb8aa3b, v25
	v_exp_f32_e32 v27, v21
	v_bitop3_b32 v85, v93, s20, v91 bitop3:0xc8
	v_or_b32_sdwa v82, v92, v90 dst_sel:WORD_1 dst_unused:UNUSED_PAD src0_sel:DWORD src1_sel:DWORD
	v_bitop3_b32 v83, v92, s20, v90 bitop3:0xc8
	v_cvt_pk_bf16_f32 v21, v22, v23
	v_add_f32_e32 v22, 1.0, v26
	v_add_f32_e32 v23, 1.0, v27
	v_pk_mul_f32 v[26:27], v[50:51], v[84:85]
	v_lshlrev_b32_e32 v34, 16, v79
	v_pk_fma_f32 v[26:27], v[46:47], v[82:83], v[26:27]
	v_and_b32_e32 v35, 0xffff0000, v79
	v_pk_fma_f32 v[26:27], v[38:39], v[34:35], v[26:27]
	v_rcp_f32_e32 v22, v22
	v_pk_add_f32 v[26:27], v[42:43], v[26:27]
	v_rcp_f32_e32 v23, v23
	v_mul_f32_e32 v34, 0xbfb8aa3b, v26
	v_mul_f32_e32 v35, 0xbfb8aa3b, v27
	v_exp_f32_e32 v34, v34
	v_exp_f32_e32 v35, v35
	v_pk_mul_f32 v[22:23], v[24:25], v[22:23]
	v_and_b32_dpp v73, v77, v147 row_ror:1 row_mask:0xf bank_mask:0xf bound_ctrl:1
	v_add_f32_e32 v34, 1.0, v34
	v_add_f32_e32 v35, 1.0, v35
	v_rcp_f32_e32 v34, v34
	v_rcp_f32_e32 v35, v35
	v_pk_mul_f32 v[22:23], v[32:33], v[22:23]
	v_and_b32_dpp v33, v76, v146 row_ror:2 row_mask:0xf bank_mask:0xf bound_ctrl:1
	v_cvt_pk_bf16_f32 v22, v22, v23
	v_pk_mul_f32 v[24:25], v[26:27], v[34:35]
	v_and_b32_dpp v35, v76, v147 row_ror:1 row_mask:0xf bank_mask:0xf bound_ctrl:1
	v_pk_mul_f32 v[24:25], v[86:87], v[24:25]
	v_and_b32_dpp v75, v77, v146 row_ror:2 row_mask:0xf bank_mask:0xf bound_ctrl:1
	v_cvt_pk_bf16_f32 v23, v24, v25
	global_store_dwordx4 v[114:115], v[20:23], off offset:256
	v_mov_b32_e32 v24, v231
	v_and_b32_dpp v81, v78, v147 row_ror:1 row_mask:0xf bank_mask:0xf bound_ctrl:1
	v_mad_i64_i32 v[20:21], s[18:19], v153, s21, v[204:205]
	v_lshl_add_u64 v[20:21], v[20:21], 0, v[108:109]
	s_waitcnt vmcnt(1)
	v_mov_b32_e32 v20, v226
	v_mov_b32_e32 v21, v227
	v_mov_b32_e32 v22, v228
	v_mov_b32_e32 v23, v229
	s_nop 1
	v_mov_b32_dpp v27, v28 row_shr:2 row_mask:0xf bank_mask:0xf bound_ctrl:1
	v_mov_b32_dpp v25, v28 row_shr:1 row_mask:0xf bank_mask:0xf bound_ctrl:1
	v_or_b32_sdwa v32, v33, v27 dst_sel:WORD_1 dst_unused:UNUSED_PAD src0_sel:DWORD src1_sel:DWORD
	v_mov_b32_dpp v71, v29 row_shr:1 row_mask:0xf bank_mask:0xf bound_ctrl:1
	v_mov_b32_dpp v77, v30 row_shr:1 row_mask:0xf bank_mask:0xf bound_ctrl:1
	v_mov_b32_dpp v80, v30 row_shr:2 row_mask:0xf bank_mask:0xf bound_ctrl:1
	v_and_b32_dpp v78, v78, v146 row_ror:2 row_mask:0xf bank_mask:0xf bound_ctrl:1
	v_mov_b32_dpp v83, v31 row_shr:2 row_mask:0xf bank_mask:0xf bound_ctrl:1
	v_and_b32_dpp v84, v79, v147 row_ror:1 row_mask:0xf bank_mask:0xf bound_ctrl:1
	v_and_b32_dpp v79, v79, v146 row_ror:2 row_mask:0xf bank_mask:0xf bound_ctrl:1
	v_bitop3_b32 v33, v33, s20, v27 bitop3:0xc8
	v_or_b32_sdwa v26, v35, v25 dst_sel:WORD_1 dst_unused:UNUSED_PAD src0_sel:DWORD src1_sel:DWORD
	v_or_b32_sdwa v34, v73, v71 dst_sel:WORD_1 dst_unused:UNUSED_PAD src0_sel:DWORD src1_sel:DWORD
	v_or_b32_sdwa v70, v81, v77 dst_sel:WORD_1 dst_unused:UNUSED_PAD src0_sel:DWORD src1_sel:DWORD
	v_or_b32_sdwa v72, v78, v80 dst_sel:WORD_1 dst_unused:UNUSED_PAD src0_sel:DWORD src1_sel:DWORD
	v_or_b32_sdwa v76, v79, v83 dst_sel:WORD_1 dst_unused:UNUSED_PAD src0_sel:DWORD src1_sel:DWORD
	v_bitop3_b32 v27, v35, s20, v25 bitop3:0xc8
	v_bitop3_b32 v35, v73, s20, v71 bitop3:0xc8
	v_bitop3_b32 v73, v78, s20, v80 bitop3:0xc8
	v_bitop3_b32 v71, v81, s20, v77 bitop3:0xc8
	v_bitop3_b32 v77, v79, s20, v83 bitop3:0xc8
	v_mov_b32_dpp v69, v29 row_shr:2 row_mask:0xf bank_mask:0xf bound_ctrl:1
	v_or_b32_sdwa v68, v75, v69 dst_sel:WORD_1 dst_unused:UNUSED_PAD src0_sel:DWORD src1_sel:DWORD
	v_bitop3_b32 v69, v75, s20, v69 bitop3:0xc8
	v_mov_b32_dpp v82, v31 row_shr:1 row_mask:0xf bank_mask:0xf bound_ctrl:1
	v_or_b32_sdwa v74, v84, v82 dst_sel:WORD_1 dst_unused:UNUSED_PAD src0_sel:DWORD src1_sel:DWORD
	v_bitop3_b32 v75, v84, s20, v82 bitop3:0xc8
	s_mov_b64 s[18:19], -1
	s_waitcnt lgkmcnt(0)
	v_pk_mul_f32 v[78:79], v[14:15], v[24:25] op_sel_hi:[1,0]
	v_pk_mul_f32 v[14:15], v[64:65], v[32:33]
	v_pk_mul_f32 v[18:19], v[18:19], v[24:25] op_sel_hi:[1,0]
	v_pk_fma_f32 v[14:15], v[60:61], v[26:27], v[14:15]
	v_lshlrev_b32_e32 v26, 16, v28
	v_and_b32_e32 v27, 0xffff0000, v28
	v_pk_fma_f32 v[14:15], v[52:53], v[26:27], v[14:15]
	v_pk_mul_f32 v[16:17], v[16:17], v[24:25] op_sel_hi:[1,0]
	v_pk_add_f32 v[14:15], v[56:57], v[14:15]
	v_lshlrev_b32_e32 v32, 16, v29
	v_mul_f32_e32 v25, 0xbfb8aa3b, v14
	v_exp_f32_e32 v26, v25
	v_mul_f32_e32 v25, 0xbfb8aa3b, v15
	v_exp_f32_e32 v27, v25
	v_pk_mul_f32 v[24:25], v[12:13], v[24:25] op_sel_hi:[1,0]
	v_add_f32_e32 v12, 1.0, v26
	v_and_b32_e32 v33, 0xffff0000, v29
	v_add_f32_e32 v13, 1.0, v27
	v_pk_mul_f32 v[26:27], v[66:67], v[68:69]
	v_rcp_f32_e32 v12, v12
	v_pk_fma_f32 v[26:27], v[62:63], v[34:35], v[26:27]
	v_rcp_f32_e32 v13, v13
	v_pk_fma_f32 v[26:27], v[54:55], v[32:33], v[26:27]
	v_mov_b32_dpp v34, v22 row_shr:1 row_mask:0xf bank_mask:0xf bound_ctrl:1
	v_pk_add_f32 v[26:27], v[58:59], v[26:27]
	v_pk_mul_f32 v[12:13], v[14:15], v[12:13]
	v_mul_f32_e32 v32, 0xbfb8aa3b, v26
	v_mul_f32_e32 v33, 0xbfb8aa3b, v27
	v_exp_f32_e32 v32, v32
	v_exp_f32_e32 v33, v33
	v_pk_mul_f32 v[12:13], v[12:13], v[16:17]
	v_pk_mul_f32 v[16:17], v[48:49], v[72:73]
	v_add_f32_e32 v32, 1.0, v32
	v_add_f32_e32 v33, 1.0, v33
	v_rcp_f32_e32 v32, v32
	v_rcp_f32_e32 v33, v33
	v_pk_fma_f32 v[16:17], v[44:45], v[70:71], v[16:17]
	v_cvt_pk_bf16_f32 v12, v12, v13
	v_mov_b32_dpp v35, v22 row_shr:2 row_mask:0xf bank_mask:0xf bound_ctrl:1
	v_pk_mul_f32 v[14:15], v[26:27], v[32:33]
	v_lshlrev_b32_e32 v26, 16, v31
	v_pk_mul_f32 v[14:15], v[18:19], v[14:15]
	v_lshlrev_b32_e32 v18, 16, v30
	v_and_b32_e32 v19, 0xffff0000, v30
	v_pk_fma_f32 v[16:17], v[36:37], v[18:19], v[16:17]
	v_and_b32_e32 v27, 0xffff0000, v31
	v_pk_add_f32 v[16:17], v[40:41], v[16:17]
	v_mov_b32_dpp v71, v23 row_shr:2 row_mask:0xf bank_mask:0xf bound_ctrl:1
	v_mul_f32_e32 v13, 0xbfb8aa3b, v16
	v_exp_f32_e32 v18, v13
	v_mul_f32_e32 v13, 0xbfb8aa3b, v17
	v_exp_f32_e32 v19, v13
	v_cvt_pk_bf16_f32 v13, v14, v15
	v_add_f32_e32 v14, 1.0, v18
	v_rcp_f32_e32 v14, v14
	v_add_f32_e32 v15, 1.0, v19
	v_pk_mul_f32 v[18:19], v[50:51], v[76:77]
	v_rcp_f32_e32 v15, v15
	v_pk_fma_f32 v[18:19], v[46:47], v[74:75], v[18:19]
	v_mov_b32_dpp v70, v23 row_shr:1 row_mask:0xf bank_mask:0xf bound_ctrl:1
	v_pk_fma_f32 v[18:19], v[38:39], v[26:27], v[18:19]
	v_pk_mul_f32 v[14:15], v[16:17], v[14:15]
	v_pk_add_f32 v[18:19], v[42:43], v[18:19]
	v_pk_mul_f32 v[14:15], v[24:25], v[14:15]
	v_mul_f32_e32 v26, 0xbfb8aa3b, v18
	v_mul_f32_e32 v27, 0xbfb8aa3b, v19
	v_exp_f32_e32 v26, v26
	v_exp_f32_e32 v27, v27
	v_cvt_pk_bf16_f32 v14, v14, v15
	v_mov_b32_dpp v24, v29 row_ror:2 row_mask:0xf bank_mask:0xf bound_ctrl:1
	v_add_f32_e32 v26, 1.0, v26
	v_add_f32_e32 v27, 1.0, v27
	v_rcp_f32_e32 v26, v26
	v_rcp_f32_e32 v27, v27
	v_mov_b32_dpp v25, v21 row_shr:2 row_mask:0xf bank_mask:0xf bound_ctrl:1
	v_cndmask_b32_e64 v33, 0, v24, s[38:39]
	v_or_b32_sdwa v24, v33, v25 dst_sel:WORD_1 dst_unused:UNUSED_PAD src0_sel:DWORD src1_sel:DWORD
	v_pk_mul_f32 v[16:17], v[18:19], v[26:27]
	v_mov_b32_dpp v18, v29 row_ror:1 row_mask:0xf bank_mask:0xf bound_ctrl:1
	v_pk_mul_f32 v[16:17], v[78:79], v[16:17]
	v_mov_b32_dpp v26, v30 row_ror:1 row_mask:0xf bank_mask:0xf bound_ctrl:1
	v_cvt_pk_bf16_f32 v15, v16, v17
	global_store_dwordx4 v[112:113], v[12:15], off offset:256
	s_nop 1
	v_mov_b32_e32 v12, v240
	v_mov_b32_dpp v16, v28 row_ror:2 row_mask:0xf bank_mask:0xf bound_ctrl:1
	v_mov_b32_dpp v14, v28 row_ror:1 row_mask:0xf bank_mask:0xf bound_ctrl:1
	v_mov_b32_dpp v15, v20 row_shr:2 row_mask:0xf bank_mask:0xf bound_ctrl:1
	v_cndmask_b32_e64 v17, 0, v16, s[38:39]
	v_mov_b32_dpp v28, v30 row_ror:2 row_mask:0xf bank_mask:0xf bound_ctrl:1
	v_mov_b32_dpp v13, v20 row_shr:1 row_mask:0xf bank_mask:0xf bound_ctrl:1
	v_cndmask_b32_e64 v19, 0, v14, s[36:37]
	v_or_b32_sdwa v16, v17, v15 dst_sel:WORD_1 dst_unused:UNUSED_PAD src0_sel:DWORD src1_sel:DWORD
	v_mov_b32_dpp v27, v21 row_shr:1 row_mask:0xf bank_mask:0xf bound_ctrl:1
	v_cndmask_b32_e64 v29, 0, v18, s[36:37]
	v_cndmask_b32_e64 v68, 0, v26, s[36:37]
	v_cndmask_b32_e64 v69, 0, v28, s[38:39]
	v_bitop3_b32 v17, v17, s20, v15 bitop3:0xc8
	v_or_b32_sdwa v14, v19, v13 dst_sel:WORD_1 dst_unused:UNUSED_PAD src0_sel:DWORD src1_sel:DWORD
	v_or_b32_sdwa v18, v29, v27 dst_sel:WORD_1 dst_unused:UNUSED_PAD src0_sel:DWORD src1_sel:DWORD
	v_or_b32_sdwa v26, v68, v34 dst_sel:WORD_1 dst_unused:UNUSED_PAD src0_sel:DWORD src1_sel:DWORD
	v_or_b32_sdwa v28, v69, v35 dst_sel:WORD_1 dst_unused:UNUSED_PAD src0_sel:DWORD src1_sel:DWORD
	v_bitop3_b32 v15, v19, s20, v13 bitop3:0xc8
	v_bitop3_b32 v19, v29, s20, v27 bitop3:0xc8
	v_bitop3_b32 v29, v69, s20, v35 bitop3:0xc8
	v_bitop3_b32 v27, v68, s20, v34 bitop3:0xc8
	v_bitop3_b32 v25, v33, s20, v25 bitop3:0xc8
	v_mov_b32_dpp v30, v31 row_ror:1 row_mask:0xf bank_mask:0xf bound_ctrl:1
	v_mov_b32_dpp v31, v31 row_ror:2 row_mask:0xf bank_mask:0xf bound_ctrl:1
	v_cndmask_b32_e64 v31, 0, v31, s[38:39]
	v_cndmask_b32_e64 v72, 0, v30, s[36:37]
	v_or_b32_sdwa v32, v31, v71 dst_sel:WORD_1 dst_unused:UNUSED_PAD src0_sel:DWORD src1_sel:DWORD
	v_bitop3_b32 v33, v31, s20, v71 bitop3:0xc8
	v_or_b32_sdwa v30, v72, v70 dst_sel:WORD_1 dst_unused:UNUSED_PAD src0_sel:DWORD src1_sel:DWORD
	v_bitop3_b32 v31, v72, s20, v70 bitop3:0xc8
	s_waitcnt lgkmcnt(0)
	v_pk_mul_f32 v[34:35], v[6:7], v[12:13] op_sel_hi:[1,0]
	v_pk_mul_f32 v[6:7], v[64:65], v[16:17]
	v_pk_mul_f32 v[10:11], v[10:11], v[12:13] op_sel_hi:[1,0]
	v_pk_fma_f32 v[6:7], v[60:61], v[14:15], v[6:7]
	v_lshlrev_b32_e32 v14, 16, v20
	v_and_b32_e32 v15, 0xffff0000, v20
	v_pk_fma_f32 v[6:7], v[52:53], v[14:15], v[6:7]
	v_pk_mul_f32 v[8:9], v[8:9], v[12:13] op_sel_hi:[1,0]
	v_pk_add_f32 v[6:7], v[56:57], v[6:7]
	v_lshlrev_b32_e32 v16, 16, v21
	v_mul_f32_e32 v13, 0xbfb8aa3b, v6
	v_exp_f32_e32 v14, v13
	v_mul_f32_e32 v13, 0xbfb8aa3b, v7
	v_exp_f32_e32 v15, v13
	v_pk_mul_f32 v[12:13], v[4:5], v[12:13] op_sel_hi:[1,0]
	v_add_f32_e32 v4, 1.0, v14
	v_and_b32_e32 v17, 0xffff0000, v21
	v_add_f32_e32 v5, 1.0, v15
	v_pk_mul_f32 v[14:15], v[66:67], v[24:25]
	v_rcp_f32_e32 v4, v4
	v_pk_fma_f32 v[14:15], v[62:63], v[18:19], v[14:15]
	v_rcp_f32_e32 v5, v5
	v_pk_fma_f32 v[14:15], v[54:55], v[16:17], v[14:15]
	v_pk_mul_f32 v[4:5], v[6:7], v[4:5]
	v_pk_add_f32 v[14:15], v[58:59], v[14:15]
	v_pk_mul_f32 v[4:5], v[4:5], v[8:9]
	v_mul_f32_e32 v16, 0xbfb8aa3b, v14
	v_mul_f32_e32 v17, 0xbfb8aa3b, v15
	v_exp_f32_e32 v16, v16
	v_exp_f32_e32 v17, v17
	v_pk_mul_f32 v[8:9], v[48:49], v[28:29]
	v_cvt_pk_bf16_f32 v4, v4, v5
	v_add_f32_e32 v16, 1.0, v16
	v_add_f32_e32 v17, 1.0, v17
	v_rcp_f32_e32 v16, v16
	v_rcp_f32_e32 v17, v17
	v_pk_fma_f32 v[8:9], v[44:45], v[26:27], v[8:9]
	v_pk_mul_f32 v[6:7], v[14:15], v[16:17]
	s_nop 0
	v_pk_mul_f32 v[6:7], v[10:11], v[6:7]
	v_lshlrev_b32_e32 v10, 16, v22
	v_and_b32_e32 v11, 0xffff0000, v22
	v_pk_fma_f32 v[8:9], v[36:37], v[10:11], v[8:9]
	v_lshlrev_b32_e32 v14, 16, v23
	v_pk_add_f32 v[8:9], v[40:41], v[8:9]
	v_and_b32_e32 v15, 0xffff0000, v23
	v_mul_f32_e32 v5, 0xbfb8aa3b, v8
	v_exp_f32_e32 v10, v5
	v_mul_f32_e32 v5, 0xbfb8aa3b, v9
	v_exp_f32_e32 v11, v5
	v_cvt_pk_bf16_f32 v5, v6, v7
	v_add_f32_e32 v6, 1.0, v10
	v_rcp_f32_e32 v6, v6
	v_add_f32_e32 v7, 1.0, v11
	v_pk_mul_f32 v[10:11], v[50:51], v[32:33]
	v_rcp_f32_e32 v7, v7
	v_pk_fma_f32 v[10:11], v[46:47], v[30:31], v[10:11]
	v_pk_mul_f32 v[6:7], v[8:9], v[6:7]
	v_pk_fma_f32 v[10:11], v[38:39], v[14:15], v[10:11]
	v_pk_mul_f32 v[6:7], v[12:13], v[6:7]
	v_pk_add_f32 v[10:11], v[42:43], v[10:11]
	v_cvt_pk_bf16_f32 v6, v6, v7
	v_mul_f32_e32 v14, 0xbfb8aa3b, v10
	v_mul_f32_e32 v15, 0xbfb8aa3b, v11
	v_exp_f32_e32 v14, v14
	v_exp_f32_e32 v15, v15
	v_add_f32_e32 v14, 1.0, v14
	v_add_f32_e32 v15, 1.0, v15
	v_rcp_f32_e32 v14, v14
	v_rcp_f32_e32 v15, v15
	s_nop 0
	v_pk_mul_f32 v[8:9], v[10:11], v[14:15]
	s_nop 0
	v_pk_mul_f32 v[8:9], v[34:35], v[8:9]
	s_nop 0
	v_cvt_pk_bf16_f32 v7, v8, v9
	global_store_dwordx4 v[110:111], v[4:7], off offset:256
	s_cbranch_vccnz .LBB0_1916
	s_andn2_b64 vcc, exec, s[0:1]
	s_cbranch_vccnz .LBB0_1915
	s_barrier
	s_branch .LBB0_1915
.LBB0_1926:
	s_waitcnt vmcnt(0)
	s_movk_i32 s20, 0x110
	v_mov_b32_e32 v241, 0x358637bd
	v_mov_b32_e32 v226, 0x44ffe000
	v_mov_b32_e32 v227, 0x3b808081
	v_mov_b32_e32 v228, 1
	v_mov_b32_e32 v229, 0xff800000
	v_mbcnt_lo_u32_b32 v251, -1, 0
	v_mbcnt_hi_u32_b32 v230, -1, v251
	v_mov_b32_e32 v231, 64
	v_mov_b32_e32 v240, 0x43e00000
	s_barrier
